# v11 + P13 EpiFin epilogue: pp/x3 loads issued three row-groups ahead into shadow registers with counted waits (was 8 serialized load groups per tile)
# speedup vs baseline: 1.0082x; 1.0005x over previous
.LBB0_1482:
	s_lshl_b32 s2, s5, 5
	s_lshl_b32 s1, s0, 8
	s_lshl_b32 s3, s4, 8
	s_or_b32 s2, s3, s2
	v_add_u32_e32 v18, s1, v189
	v_or_b32_e32 v2, s2, v1
	v_ashrrev_i32_e32 v19, 31, v18
	v_ashrrev_i32_e32 v3, 31, v2
	v_lshlrev_b64 v[4:5], 11, v[18:19]
	v_lshl_add_u64 v[20:21], v[4:5], 0, v[2:3]
	v_lshlrev_b64 v[4:5], 1, v[20:21]
	v_lshl_add_u64 v[14:15], s[18:19], 0, v[4:5]
	s_barrier
	global_load_dwordx4 v[6:9], v[14:15], off
	v_lshl_add_u64 v[4:5], s[16:17], 0, v[4:5]
	global_load_dwordx4 v[10:13], v[4:5], off
	s_nop 0
	global_load_dwordx4 v[14:17], v[14:15], off offset:256
	s_nop 0
	global_load_dwordx4 v[30:33], v[4:5], off offset:256
	v_lshlrev_b64 v[254:255], 11, v[18:19]
	v_lshl_add_u64 v[254:255], v[254:255], 0, v[2:3]
	v_lshlrev_b64 v[254:255], 1, v[254:255]
	v_mov_b32_e32 v250, 0x10000
	v_mov_b32_e32 v251, 0
	v_lshl_add_u64 v[196:197], s[16:17], 0, v[254:255]
	v_lshl_add_u64 v[254:255], s[18:19], 0, v[254:255]
	v_lshl_add_u64 v[254:255], v[254:255], 0, v[250:251]
	v_lshl_add_u64 v[196:197], v[196:197], 0, v[250:251]
	global_load_dwordx4 v[200:203], v[254:255], off
	global_load_dwordx4 v[204:207], v[196:197], off
	global_load_dwordx4 v[208:211], v[254:255], off offset:256
	global_load_dwordx4 v[212:215], v[196:197], off offset:256
	v_lshl_add_u64 v[254:255], v[254:255], 0, v[250:251]
	v_lshl_add_u64 v[196:197], v[196:197], 0, v[250:251]
	global_load_dwordx4 v[216:219], v[254:255], off
	global_load_dwordx4 v[220:223], v[196:197], off
	global_load_dwordx4 v[224:227], v[254:255], off offset:256
	global_load_dwordx4 v[228:231], v[196:197], off offset:256
	v_lshl_add_u64 v[254:255], v[254:255], 0, v[250:251]
	v_lshl_add_u64 v[196:197], v[196:197], 0, v[250:251]
	global_load_dwordx4 v[232:235], v[254:255], off
	global_load_dwordx4 v[236:239], v[196:197], off
	global_load_dwordx4 v[240:243], v[254:255], off offset:256
	global_load_dwordx4 v[244:247], v[196:197], off offset:256
	v_mbcnt_lo_u32_b32 v4, -1, 0
	s_mov_b32 s6, 0x3c800000
	s_mov_b32 s2, 0xbfb8aa3b
	v_mbcnt_hi_u32_b32 v163, -1, v4
	v_pk_mul_f32 v[4:5], v[160:161], s[6:7] op_sel_hi:[1,0]
	v_pk_mul_f32 v[22:23], v[158:159], s[6:7] op_sel_hi:[1,0]
	v_pk_mul_f32 v[24:25], v[156:157], s[6:7] op_sel_hi:[1,0]
	v_pk_mul_f32 v[26:27], v[154:155], s[6:7] op_sel_hi:[1,0]
	v_and_b32_e32 v28, 64, v163
	v_pk_mul_f32 v[22:23], v[22:23], s[2:3] op_sel_hi:[1,0]
	v_pk_mul_f32 v[4:5], v[4:5], s[2:3] op_sel_hi:[1,0]
	v_pk_mul_f32 v[26:27], v[26:27], s[2:3] op_sel_hi:[1,0]
	v_pk_mul_f32 v[24:25], v[24:25], s[2:3] op_sel_hi:[1,0]
	v_add_u32_e32 v165, 64, v28
	v_exp_f32_e32 v22, v22
	v_exp_f32_e32 v23, v23
	v_exp_f32_e32 v28, v4
	v_exp_f32_e32 v29, v5
	v_exp_f32_e32 v26, v26
	v_exp_f32_e32 v27, v27
	v_exp_f32_e32 v24, v24
	v_exp_f32_e32 v25, v25
	v_xor_b32_e32 v154, 16, v163
	v_cmp_lt_i32_e32 vcc, v154, v165
	v_pk_add_f32 v[22:23], v[22:23], 1.0 op_sel_hi:[1,0]
	v_pk_add_f32 v[28:29], v[28:29], 1.0 op_sel_hi:[1,0]
	v_pk_add_f32 v[26:27], v[26:27], 1.0 op_sel_hi:[1,0]
	v_pk_add_f32 v[24:25], v[24:25], 1.0 op_sel_hi:[1,0]
	v_cndmask_b32_e32 v4, v163, v154, vcc
	v_rcp_f32_e32 v22, v22
	v_rcp_f32_e32 v23, v23
	v_rcp_f32_e32 v28, v28
	v_rcp_f32_e32 v29, v29
	v_rcp_f32_e32 v26, v26
	v_rcp_f32_e32 v27, v27
	v_rcp_f32_e32 v154, v24
	v_rcp_f32_e32 v155, v25
	v_pk_mul_f32 v[148:149], v[148:149], s[6:7] op_sel_hi:[1,0]
	v_pk_mul_f32 v[146:147], v[146:147], s[6:7] op_sel_hi:[1,0]
	v_pk_mul_f32 v[148:149], v[148:149], s[2:3] op_sel_hi:[1,0]
	v_pk_mul_f32 v[146:147], v[146:147], s[2:3] op_sel_hi:[1,0]
	v_exp_f32_e32 v148, v148
	v_exp_f32_e32 v149, v149
	v_exp_f32_e32 v146, v146
	v_exp_f32_e32 v147, v147
	v_lshlrev_b32_e32 v4, 2, v4
	v_pk_add_f32 v[148:149], v[148:149], 1.0 op_sel_hi:[1,0]
	v_pk_add_f32 v[146:147], v[146:147], 1.0 op_sel_hi:[1,0]
	v_rcp_f32_e32 v148, v148
	v_rcp_f32_e32 v149, v149
	s_waitcnt vmcnt(12)
	v_lshlrev_b32_e32 v160, 16, v10
	v_lshlrev_b32_e32 v156, 16, v6
	v_and_b32_e32 v157, 0xffff0000, v6
	v_lshlrev_b32_e32 v6, 16, v7
	v_and_b32_e32 v7, 0xffff0000, v7
	v_lshlrev_b32_e32 v158, 16, v8
	v_and_b32_e32 v159, 0xffff0000, v8
	v_lshlrev_b32_e32 v8, 16, v9
	v_and_b32_e32 v9, 0xffff0000, v9
	v_and_b32_e32 v161, 0xffff0000, v10
	v_lshlrev_b32_e32 v10, 16, v11
	v_and_b32_e32 v11, 0xffff0000, v11
	v_lshlrev_b32_e32 v170, 16, v12
	v_and_b32_e32 v171, 0xffff0000, v12
	v_lshlrev_b32_e32 v12, 16, v13
	v_and_b32_e32 v13, 0xffff0000, v13
	v_pk_fma_f32 v[24:25], v[28:29], v[6:7], v[10:11]
	v_pk_fma_f32 v[28:29], v[22:23], v[156:157], v[160:161]
	v_pk_fma_f32 v[22:23], v[154:155], v[8:9], v[12:13]
	v_pk_fma_f32 v[26:27], v[26:27], v[158:159], v[170:171]
	v_mul_f32_e32 v5, v29, v29
	v_mul_f32_e32 v6, v25, v25
	v_mul_f32_e32 v7, v27, v27
	v_mul_f32_e32 v8, v23, v23
	v_fmac_f32_e32 v5, v28, v28
	v_fmac_f32_e32 v6, v24, v24
	v_fmac_f32_e32 v7, v26, v26
	v_fmac_f32_e32 v8, v22, v22
	v_add_f32_e32 v5, v5, v6
	v_add_f32_e32 v6, v7, v8
	v_lshlrev_b32_e32 v174, 16, v16
	v_and_b32_e32 v175, 0xffff0000, v16
	v_add_f32_e32 v5, v5, v6
	v_lshlrev_b32_e32 v6, 16, v17
	v_and_b32_e32 v7, 0xffff0000, v17
	v_lshlrev_b32_e32 v8, 16, v30
	v_and_b32_e32 v9, 0xffff0000, v30
	v_lshlrev_b32_e32 v10, 16, v31
	v_and_b32_e32 v11, 0xffff0000, v31
	v_lshlrev_b32_e32 v12, 16, v32
	v_and_b32_e32 v13, 0xffff0000, v32
	v_lshlrev_b32_e32 v16, 16, v33
	v_and_b32_e32 v17, 0xffff0000, v33
	v_pk_mul_f32 v[30:31], v[152:153], s[6:7] op_sel_hi:[1,0]
	v_pk_mul_f32 v[32:33], v[150:151], s[6:7] op_sel_hi:[1,0]
	v_pk_mul_f32 v[30:31], v[30:31], s[2:3] op_sel_hi:[1,0]
	v_pk_mul_f32 v[32:33], v[32:33], s[2:3] op_sel_hi:[1,0]
	v_exp_f32_e32 v30, v30
	v_exp_f32_e32 v32, v32
	v_exp_f32_e32 v33, v33
	v_exp_f32_e32 v31, v31
	v_rcp_f32_e32 v150, v146
	v_rcp_f32_e32 v151, v147
	v_pk_add_f32 v[32:33], v[32:33], 1.0 op_sel_hi:[1,0]
	v_pk_add_f32 v[30:31], v[30:31], 1.0 op_sel_hi:[1,0]
	v_rcp_f32_e32 v32, v32
	v_rcp_f32_e32 v33, v33
	v_rcp_f32_e32 v30, v30
	v_rcp_f32_e32 v31, v31
	v_lshlrev_b32_e32 v172, 16, v14
	v_and_b32_e32 v173, 0xffff0000, v14
	v_lshlrev_b32_e32 v14, 16, v15
	v_and_b32_e32 v15, 0xffff0000, v15
	v_pk_fma_f32 v[30:31], v[30:31], v[14:15], v[10:11]
	v_pk_fma_f32 v[32:33], v[32:33], v[172:173], v[8:9]
	v_pk_fma_f32 v[146:147], v[148:149], v[6:7], v[16:17]
	v_mul_f32_e32 v6, v33, v33
	v_mul_f32_e32 v7, v31, v31
	v_pk_fma_f32 v[148:149], v[150:151], v[174:175], v[12:13]
	v_fmac_f32_e32 v6, v32, v32
	v_fmac_f32_e32 v7, v30, v30
	v_add_f32_e32 v6, v6, v7
	v_mul_f32_e32 v7, v149, v149
	v_mul_f32_e32 v8, v147, v147
	v_fmac_f32_e32 v7, v148, v148
	v_fmac_f32_e32 v8, v146, v146
	v_add_f32_e32 v7, v7, v8
	v_add_f32_e32 v6, v6, v7
	v_add_f32_e32 v5, v5, v6
	ds_bpermute_b32 v7, v4, v5
	v_xor_b32_e32 v6, 32, v163
	v_cmp_lt_i32_e32 vcc, v6, v165
	s_lshl_b32 s3, s5, 2
	s_add_i32 s5, s3, 0
	v_cndmask_b32_e32 v6, v163, v6, vcc
	v_lshlrev_b32_e32 v6, 2, v6
	s_waitcnt lgkmcnt(0)
	v_add_f32_e32 v7, v5, v7
	ds_bpermute_b32 v8, v6, v7
	v_cmp_gt_u32_e32 vcc, 16, v198
	v_lshl_add_u32 v5, v189, 4, s5
	s_and_saveexec_b64 s[20:21], vcc
	s_cbranch_execz .LBB0_1484
	s_waitcnt lgkmcnt(0)
	v_add_f32_e32 v7, v7, v8
	ds_write_b32 v5, v7
.LBB0_1484:
	s_or_b64 exec, exec, s[20:21]
	s_waitcnt lgkmcnt(0)
	s_waitcnt vmcnt(8)
	v_mov_b64_e32 v[8:9], v[200:201]
	v_mov_b64_e32 v[10:11], v[202:203]
	v_mov_b64_e32 v[12:13], v[204:205]
	v_mov_b64_e32 v[14:15], v[206:207]
	v_mov_b64_e32 v[150:151], v[208:209]
	v_mov_b64_e32 v[152:153], v[210:211]
	v_mov_b64_e32 v[154:155], v[212:213]
	v_mov_b64_e32 v[156:157], v[214:215]
	v_lshl_add_u64 v[254:255], v[254:255], 0, v[250:251]
	v_lshl_add_u64 v[196:197], v[196:197], 0, v[250:251]
	v_lshl_add_u64 v[254:255], v[254:255], 0, v[250:251]
	v_lshl_add_u64 v[196:197], v[196:197], 0, v[250:251]
	v_lshl_add_u64 v[254:255], v[254:255], 0, v[250:251]
	v_lshl_add_u64 v[196:197], v[196:197], 0, v[250:251]
	v_lshl_add_u64 v[254:255], v[254:255], 0, v[250:251]
	v_lshl_add_u64 v[196:197], v[196:197], 0, v[250:251]
	v_lshl_add_u64 v[254:255], v[254:255], 0, v[250:251]
	v_lshl_add_u64 v[196:197], v[196:197], 0, v[250:251]
	global_load_dwordx4 v[200:203], v[254:255], off
	global_load_dwordx4 v[204:207], v[196:197], off
	global_load_dwordx4 v[208:211], v[254:255], off offset:256
	global_load_dwordx4 v[212:215], v[196:197], off offset:256
	v_pk_mul_f32 v[16:17], v[144:145], s[6:7] op_sel_hi:[1,0]
	v_pk_mul_f32 v[142:143], v[142:143], s[6:7] op_sel_hi:[1,0]
	v_pk_mul_f32 v[140:141], v[140:141], s[6:7] op_sel_hi:[1,0]
	v_pk_mul_f32 v[138:139], v[138:139], s[6:7] op_sel_hi:[1,0]
	v_pk_mul_f32 v[136:137], v[136:137], s[6:7] op_sel_hi:[1,0]
	v_pk_mul_f32 v[142:143], v[142:143], s[2:3] op_sel_hi:[1,0]
	v_pk_mul_f32 v[16:17], v[16:17], s[2:3] op_sel_hi:[1,0]
	v_pk_mul_f32 v[138:139], v[138:139], s[2:3] op_sel_hi:[1,0]
	v_pk_mul_f32 v[140:141], v[140:141], s[2:3] op_sel_hi:[1,0]
	v_pk_mul_f32 v[144:145], v[136:137], s[2:3] op_sel_hi:[1,0]
	v_exp_f32_e32 v136, v142
	v_exp_f32_e32 v137, v143
	v_exp_f32_e32 v16, v16
	v_exp_f32_e32 v17, v17
	v_exp_f32_e32 v138, v138
	v_exp_f32_e32 v139, v139
	v_exp_f32_e32 v140, v140
	v_exp_f32_e32 v141, v141
	v_pk_mul_f32 v[134:135], v[134:135], s[6:7] op_sel_hi:[1,0]
	v_pk_add_f32 v[16:17], v[16:17], 1.0 op_sel_hi:[1,0]
	v_pk_mul_f32 v[134:135], v[134:135], s[2:3] op_sel_hi:[1,0]
	v_rcp_f32_e32 v16, v16
	v_exp_f32_e32 v142, v134
	v_exp_f32_e32 v143, v135
	v_pk_add_f32 v[134:135], v[136:137], 1.0 op_sel_hi:[1,0]
	v_pk_add_f32 v[136:137], v[138:139], 1.0 op_sel_hi:[1,0]
	v_pk_add_f32 v[138:139], v[140:141], 1.0 op_sel_hi:[1,0]
	v_rcp_f32_e32 v134, v134
	v_rcp_f32_e32 v135, v135
	v_rcp_f32_e32 v17, v17
	v_rcp_f32_e32 v158, v136
	v_rcp_f32_e32 v159, v137
	v_rcp_f32_e32 v138, v138
	v_rcp_f32_e32 v139, v139
	v_lshlrev_b32_e32 v170, 16, v12
	v_lshlrev_b32_e32 v140, 16, v8
	v_and_b32_e32 v141, 0xffff0000, v8
	v_lshlrev_b32_e32 v8, 16, v9
	v_and_b32_e32 v9, 0xffff0000, v9
	v_lshlrev_b32_e32 v160, 16, v10
	v_and_b32_e32 v161, 0xffff0000, v10
	v_lshlrev_b32_e32 v10, 16, v11
	v_and_b32_e32 v11, 0xffff0000, v11
	v_and_b32_e32 v171, 0xffff0000, v12
	v_lshlrev_b32_e32 v12, 16, v13
	v_and_b32_e32 v13, 0xffff0000, v13
	v_lshlrev_b32_e32 v172, 16, v14
	v_and_b32_e32 v173, 0xffff0000, v14
	v_lshlrev_b32_e32 v14, 16, v15
	v_and_b32_e32 v15, 0xffff0000, v15
	v_pk_fma_f32 v[136:137], v[16:17], v[8:9], v[12:13]
	v_pk_fma_f32 v[140:141], v[134:135], v[140:141], v[170:171]
	v_pk_fma_f32 v[134:135], v[138:139], v[10:11], v[14:15]
	v_pk_fma_f32 v[138:139], v[158:159], v[160:161], v[172:173]
	v_mul_f32_e32 v7, v141, v141
	v_mul_f32_e32 v8, v137, v137
	v_mul_f32_e32 v9, v139, v139
	v_mul_f32_e32 v10, v135, v135
	v_fmac_f32_e32 v7, v140, v140
	v_fmac_f32_e32 v8, v136, v136
	v_fmac_f32_e32 v9, v138, v138
	v_fmac_f32_e32 v10, v134, v134
	v_add_f32_e32 v7, v7, v8
	v_add_f32_e32 v8, v9, v10
	v_add_f32_e32 v7, v7, v8
	v_exp_f32_e32 v8, v144
	v_exp_f32_e32 v9, v145
	v_pk_mul_f32 v[12:13], v[132:133], s[6:7] op_sel_hi:[1,0]
	v_pk_mul_f32 v[14:15], v[130:131], s[6:7] op_sel_hi:[1,0]
	v_pk_mul_f32 v[12:13], v[12:13], s[2:3] op_sel_hi:[1,0]
	v_pk_mul_f32 v[14:15], v[14:15], s[2:3] op_sel_hi:[1,0]
	v_exp_f32_e32 v12, v12
	v_exp_f32_e32 v14, v14
	v_exp_f32_e32 v15, v15
	v_exp_f32_e32 v13, v13
	v_pk_add_f32 v[10:11], v[142:143], 1.0 op_sel_hi:[1,0]
	v_pk_add_f32 v[8:9], v[8:9], 1.0 op_sel_hi:[1,0]
	v_rcp_f32_e32 v10, v10
	v_rcp_f32_e32 v11, v11
	v_rcp_f32_e32 v8, v8
	v_rcp_f32_e32 v9, v9
	v_pk_add_f32 v[14:15], v[14:15], 1.0 op_sel_hi:[1,0]
	v_pk_add_f32 v[12:13], v[12:13], 1.0 op_sel_hi:[1,0]
	v_rcp_f32_e32 v14, v14
	v_rcp_f32_e32 v12, v12
	v_rcp_f32_e32 v13, v13
	v_rcp_f32_e32 v15, v15
	v_lshlrev_b32_e32 v174, 16, v150
	v_and_b32_e32 v175, 0xffff0000, v150
	v_lshlrev_b32_e32 v150, 16, v151
	v_and_b32_e32 v151, 0xffff0000, v151
	v_lshlrev_b32_e32 v178, 16, v154
	v_and_b32_e32 v179, 0xffff0000, v154
	v_lshlrev_b32_e32 v154, 16, v155
	v_and_b32_e32 v155, 0xffff0000, v155
	v_pk_fma_f32 v[130:131], v[8:9], v[150:151], v[154:155]
	v_pk_fma_f32 v[132:133], v[10:11], v[174:175], v[178:179]
	v_lshlrev_b32_e32 v176, 16, v152
	v_and_b32_e32 v177, 0xffff0000, v152
	v_lshlrev_b32_e32 v152, 16, v153
	v_and_b32_e32 v153, 0xffff0000, v153
	v_lshlrev_b32_e32 v180, 16, v156
	v_and_b32_e32 v181, 0xffff0000, v156
	v_lshlrev_b32_e32 v156, 16, v157
	v_and_b32_e32 v157, 0xffff0000, v157
	v_mul_f32_e32 v8, v133, v133
	v_mul_f32_e32 v9, v131, v131
	v_pk_fma_f32 v[142:143], v[12:13], v[152:153], v[156:157]
	v_pk_fma_f32 v[144:145], v[14:15], v[176:177], v[180:181]
	v_fmac_f32_e32 v8, v132, v132
	v_fmac_f32_e32 v9, v130, v130
	v_add_f32_e32 v8, v8, v9
	v_mul_f32_e32 v9, v145, v145
	v_mul_f32_e32 v10, v143, v143
	v_fmac_f32_e32 v9, v144, v144
	v_fmac_f32_e32 v10, v142, v142
	v_add_f32_e32 v9, v9, v10
	v_add_f32_e32 v8, v8, v9
	v_add_f32_e32 v7, v7, v8
	ds_bpermute_b32 v8, v4, v7
	s_waitcnt lgkmcnt(0)
	v_add_f32_e32 v7, v7, v8
	ds_bpermute_b32 v8, v6, v7
	s_and_saveexec_b64 s[2:3], vcc
	s_cbranch_execz .LBB0_1486
	s_waitcnt lgkmcnt(0)
	v_add_f32_e32 v7, v7, v8
	ds_write_b32 v5, v7 offset:256
.LBB0_1486:
	s_or_b64 exec, exec, s[2:3]
	s_waitcnt lgkmcnt(0)
	s_waitcnt vmcnt(8)
	v_mov_b64_e32 v[8:9], v[216:217]
	v_mov_b64_e32 v[10:11], v[218:219]
	v_mov_b64_e32 v[12:13], v[220:221]
	v_mov_b64_e32 v[14:15], v[222:223]
	v_mov_b64_e32 v[150:151], v[224:225]
	v_mov_b64_e32 v[152:153], v[226:227]
	v_mov_b64_e32 v[154:155], v[228:229]
	v_mov_b64_e32 v[156:157], v[230:231]
	v_lshl_add_u64 v[254:255], v[254:255], 0, v[250:251]
	v_lshl_add_u64 v[196:197], v[196:197], 0, v[250:251]
	global_load_dwordx4 v[216:219], v[254:255], off
	global_load_dwordx4 v[220:223], v[196:197], off
	global_load_dwordx4 v[224:227], v[254:255], off offset:256
	global_load_dwordx4 v[228:231], v[196:197], off offset:256
	s_mov_b32 s2, 0xbfb8aa3b
	v_pk_mul_f32 v[16:17], v[128:129], s[6:7] op_sel_hi:[1,0]
	v_pk_mul_f32 v[126:127], v[126:127], s[6:7] op_sel_hi:[1,0]
	v_pk_mul_f32 v[124:125], v[124:125], s[6:7] op_sel_hi:[1,0]
	v_pk_mul_f32 v[122:123], v[122:123], s[6:7] op_sel_hi:[1,0]
	v_pk_mul_f32 v[128:129], v[120:121], s[6:7] op_sel_hi:[1,0]
	v_pk_mul_f32 v[118:119], v[118:119], s[6:7] op_sel_hi:[1,0]
	v_pk_mul_f32 v[120:121], v[126:127], s[2:3] op_sel_hi:[1,0]
	v_pk_mul_f32 v[16:17], v[16:17], s[2:3] op_sel_hi:[1,0]
	v_pk_mul_f32 v[122:123], v[122:123], s[2:3] op_sel_hi:[1,0]
	v_pk_mul_f32 v[124:125], v[124:125], s[2:3] op_sel_hi:[1,0]
	v_pk_mul_f32 v[126:127], v[118:119], s[2:3] op_sel_hi:[1,0]
	v_exp_f32_e32 v118, v120
	v_exp_f32_e32 v119, v121
	v_exp_f32_e32 v16, v16
	v_exp_f32_e32 v17, v17
	v_exp_f32_e32 v120, v122
	v_exp_f32_e32 v121, v123
	v_exp_f32_e32 v122, v124
	v_exp_f32_e32 v123, v125
	v_pk_add_f32 v[118:119], v[118:119], 1.0 op_sel_hi:[1,0]
	v_pk_add_f32 v[16:17], v[16:17], 1.0 op_sel_hi:[1,0]
	v_pk_add_f32 v[120:121], v[120:121], 1.0 op_sel_hi:[1,0]
	v_pk_add_f32 v[122:123], v[122:123], 1.0 op_sel_hi:[1,0]
	v_rcp_f32_e32 v118, v118
	v_rcp_f32_e32 v119, v119
	v_rcp_f32_e32 v16, v16
	v_rcp_f32_e32 v17, v17
	v_rcp_f32_e32 v158, v120
	v_rcp_f32_e32 v159, v121
	v_rcp_f32_e32 v122, v122
	v_rcp_f32_e32 v123, v123
	v_exp_f32_e32 v126, v126
	v_exp_f32_e32 v127, v127
	v_lshlrev_b32_e32 v170, 16, v12
	v_lshlrev_b32_e32 v124, 16, v8
	v_and_b32_e32 v125, 0xffff0000, v8
	v_lshlrev_b32_e32 v8, 16, v9
	v_and_b32_e32 v9, 0xffff0000, v9
	v_lshlrev_b32_e32 v160, 16, v10
	v_and_b32_e32 v161, 0xffff0000, v10
	v_lshlrev_b32_e32 v10, 16, v11
	v_and_b32_e32 v11, 0xffff0000, v11
	v_and_b32_e32 v171, 0xffff0000, v12
	v_lshlrev_b32_e32 v12, 16, v13
	v_and_b32_e32 v13, 0xffff0000, v13
	v_lshlrev_b32_e32 v172, 16, v14
	v_and_b32_e32 v173, 0xffff0000, v14
	v_lshlrev_b32_e32 v14, 16, v15
	v_and_b32_e32 v15, 0xffff0000, v15
	v_pk_fma_f32 v[120:121], v[16:17], v[8:9], v[12:13]
	v_pk_fma_f32 v[124:125], v[118:119], v[124:125], v[170:171]
	v_pk_fma_f32 v[118:119], v[122:123], v[10:11], v[14:15]
	v_pk_fma_f32 v[122:123], v[158:159], v[160:161], v[172:173]
	v_mul_f32_e32 v7, v125, v125
	v_mul_f32_e32 v8, v121, v121
	v_mul_f32_e32 v9, v123, v123
	v_mul_f32_e32 v10, v119, v119
	v_fmac_f32_e32 v7, v124, v124
	v_fmac_f32_e32 v8, v120, v120
	v_fmac_f32_e32 v9, v122, v122
	v_fmac_f32_e32 v10, v118, v118
	v_add_f32_e32 v7, v7, v8
	v_add_f32_e32 v8, v9, v10
	v_add_f32_e32 v7, v7, v8
	v_pk_mul_f32 v[8:9], v[128:129], s[2:3] op_sel_hi:[1,0]
	v_pk_mul_f32 v[12:13], v[116:117], s[6:7] op_sel_hi:[1,0]
	v_exp_f32_e32 v8, v8
	v_exp_f32_e32 v9, v9
	v_pk_mul_f32 v[14:15], v[114:115], s[6:7] op_sel_hi:[1,0]
	v_pk_mul_f32 v[12:13], v[12:13], s[2:3] op_sel_hi:[1,0]
	v_pk_mul_f32 v[14:15], v[14:15], s[2:3] op_sel_hi:[1,0]
	v_exp_f32_e32 v12, v12
	v_exp_f32_e32 v14, v14
	v_exp_f32_e32 v15, v15
	v_exp_f32_e32 v13, v13
	v_pk_add_f32 v[10:11], v[126:127], 1.0 op_sel_hi:[1,0]
	v_pk_add_f32 v[8:9], v[8:9], 1.0 op_sel_hi:[1,0]
	v_rcp_f32_e32 v10, v10
	v_rcp_f32_e32 v11, v11
	v_rcp_f32_e32 v8, v8
	v_rcp_f32_e32 v9, v9
	v_pk_add_f32 v[14:15], v[14:15], 1.0 op_sel_hi:[1,0]
	v_pk_add_f32 v[12:13], v[12:13], 1.0 op_sel_hi:[1,0]
	v_rcp_f32_e32 v14, v14
	v_rcp_f32_e32 v12, v12
	v_rcp_f32_e32 v13, v13
	v_rcp_f32_e32 v15, v15
	v_lshlrev_b32_e32 v174, 16, v150
	v_and_b32_e32 v175, 0xffff0000, v150
	v_lshlrev_b32_e32 v150, 16, v151
	v_and_b32_e32 v151, 0xffff0000, v151
	v_lshlrev_b32_e32 v178, 16, v154
	v_and_b32_e32 v179, 0xffff0000, v154
	v_lshlrev_b32_e32 v154, 16, v155
	v_and_b32_e32 v155, 0xffff0000, v155
	v_pk_fma_f32 v[114:115], v[8:9], v[150:151], v[154:155]
	v_pk_fma_f32 v[116:117], v[10:11], v[174:175], v[178:179]
	v_lshlrev_b32_e32 v176, 16, v152
	v_and_b32_e32 v177, 0xffff0000, v152
	v_lshlrev_b32_e32 v152, 16, v153
	v_and_b32_e32 v153, 0xffff0000, v153
	v_lshlrev_b32_e32 v180, 16, v156
	v_and_b32_e32 v181, 0xffff0000, v156
	v_lshlrev_b32_e32 v156, 16, v157
	v_and_b32_e32 v157, 0xffff0000, v157
	v_mul_f32_e32 v8, v117, v117
	v_mul_f32_e32 v9, v115, v115
	v_pk_fma_f32 v[126:127], v[12:13], v[152:153], v[156:157]
	v_pk_fma_f32 v[128:129], v[14:15], v[176:177], v[180:181]
	v_fmac_f32_e32 v8, v116, v116
	v_fmac_f32_e32 v9, v114, v114
	v_add_f32_e32 v8, v8, v9
	v_mul_f32_e32 v9, v129, v129
	v_mul_f32_e32 v10, v127, v127
	v_fmac_f32_e32 v9, v128, v128
	v_fmac_f32_e32 v10, v126, v126
	v_add_f32_e32 v9, v9, v10
	v_add_f32_e32 v8, v8, v9
	v_add_f32_e32 v7, v7, v8
	ds_bpermute_b32 v8, v4, v7
	s_waitcnt lgkmcnt(0)
	v_add_f32_e32 v7, v7, v8
	ds_bpermute_b32 v8, v6, v7
	s_and_saveexec_b64 s[20:21], vcc
	s_cbranch_execz .LBB0_1488
	s_waitcnt lgkmcnt(0)
	v_add_f32_e32 v7, v7, v8
	ds_write_b32 v5, v7 offset:512
.LBB0_1488:
	s_or_b64 exec, exec, s[20:21]
	s_waitcnt lgkmcnt(0)
	s_waitcnt vmcnt(8)
	v_mov_b64_e32 v[8:9], v[232:233]
	v_mov_b64_e32 v[10:11], v[234:235]
	v_mov_b64_e32 v[12:13], v[236:237]
	v_mov_b64_e32 v[14:15], v[238:239]
	v_mov_b64_e32 v[150:151], v[240:241]
	v_mov_b64_e32 v[152:153], v[242:243]
	v_mov_b64_e32 v[154:155], v[244:245]
	v_mov_b64_e32 v[156:157], v[246:247]
	v_lshl_add_u64 v[254:255], v[254:255], 0, v[250:251]
	v_lshl_add_u64 v[196:197], v[196:197], 0, v[250:251]
	global_load_dwordx4 v[232:235], v[254:255], off
	global_load_dwordx4 v[236:239], v[196:197], off
	global_load_dwordx4 v[240:243], v[254:255], off offset:256
	global_load_dwordx4 v[244:247], v[196:197], off offset:256
	v_pk_mul_f32 v[16:17], v[112:113], s[6:7] op_sel_hi:[1,0]
	v_pk_mul_f32 v[110:111], v[110:111], s[6:7] op_sel_hi:[1,0]
	v_pk_mul_f32 v[108:109], v[108:109], s[6:7] op_sel_hi:[1,0]
	v_pk_mul_f32 v[106:107], v[106:107], s[6:7] op_sel_hi:[1,0]
	v_pk_mul_f32 v[104:105], v[104:105], s[6:7] op_sel_hi:[1,0]
	v_pk_mul_f32 v[110:111], v[110:111], s[2:3] op_sel_hi:[1,0]
	v_pk_mul_f32 v[16:17], v[16:17], s[2:3] op_sel_hi:[1,0]
	v_pk_mul_f32 v[106:107], v[106:107], s[2:3] op_sel_hi:[1,0]
	v_pk_mul_f32 v[108:109], v[108:109], s[2:3] op_sel_hi:[1,0]
	v_pk_mul_f32 v[112:113], v[104:105], s[2:3] op_sel_hi:[1,0]
	v_exp_f32_e32 v104, v110
	v_exp_f32_e32 v105, v111
	v_exp_f32_e32 v16, v16
	v_exp_f32_e32 v17, v17
	v_exp_f32_e32 v106, v106
	v_exp_f32_e32 v107, v107
	v_exp_f32_e32 v108, v108
	v_exp_f32_e32 v109, v109
	v_pk_mul_f32 v[102:103], v[102:103], s[6:7] op_sel_hi:[1,0]
	v_pk_add_f32 v[16:17], v[16:17], 1.0 op_sel_hi:[1,0]
	v_pk_mul_f32 v[102:103], v[102:103], s[2:3] op_sel_hi:[1,0]
	v_rcp_f32_e32 v16, v16
	v_exp_f32_e32 v110, v102
	v_exp_f32_e32 v111, v103
	v_pk_add_f32 v[102:103], v[104:105], 1.0 op_sel_hi:[1,0]
	v_pk_add_f32 v[104:105], v[106:107], 1.0 op_sel_hi:[1,0]
	v_pk_add_f32 v[106:107], v[108:109], 1.0 op_sel_hi:[1,0]
	v_rcp_f32_e32 v102, v102
	v_rcp_f32_e32 v103, v103
	v_rcp_f32_e32 v17, v17
	v_rcp_f32_e32 v104, v104
	v_rcp_f32_e32 v105, v105
	v_rcp_f32_e32 v158, v106
	v_rcp_f32_e32 v159, v107
	v_lshlrev_b32_e32 v170, 16, v12
	v_lshlrev_b32_e32 v108, 16, v8
	v_and_b32_e32 v109, 0xffff0000, v8
	v_lshlrev_b32_e32 v8, 16, v9
	v_and_b32_e32 v9, 0xffff0000, v9
	v_lshlrev_b32_e32 v160, 16, v10
	v_and_b32_e32 v161, 0xffff0000, v10
	v_lshlrev_b32_e32 v10, 16, v11
	v_and_b32_e32 v11, 0xffff0000, v11
	v_and_b32_e32 v171, 0xffff0000, v12
	v_lshlrev_b32_e32 v12, 16, v13
	v_and_b32_e32 v13, 0xffff0000, v13
	v_lshlrev_b32_e32 v172, 16, v14
	v_and_b32_e32 v173, 0xffff0000, v14
	v_lshlrev_b32_e32 v14, 16, v15
	v_and_b32_e32 v15, 0xffff0000, v15
	v_pk_fma_f32 v[106:107], v[16:17], v[8:9], v[12:13]
	v_pk_fma_f32 v[108:109], v[102:103], v[108:109], v[170:171]
	v_pk_fma_f32 v[102:103], v[158:159], v[10:11], v[14:15]
	v_pk_fma_f32 v[104:105], v[104:105], v[160:161], v[172:173]
	v_mul_f32_e32 v7, v109, v109
	v_mul_f32_e32 v8, v107, v107
	v_mul_f32_e32 v9, v105, v105
	v_mul_f32_e32 v10, v103, v103
	v_fmac_f32_e32 v7, v108, v108
	v_fmac_f32_e32 v8, v106, v106
	v_fmac_f32_e32 v9, v104, v104
	v_fmac_f32_e32 v10, v102, v102
	v_add_f32_e32 v7, v7, v8
	v_add_f32_e32 v8, v9, v10
	v_add_f32_e32 v7, v7, v8
	v_exp_f32_e32 v8, v112
	v_exp_f32_e32 v9, v113
	v_pk_mul_f32 v[12:13], v[100:101], s[6:7] op_sel_hi:[1,0]
	v_pk_mul_f32 v[14:15], v[98:99], s[6:7] op_sel_hi:[1,0]
	v_pk_mul_f32 v[12:13], v[12:13], s[2:3] op_sel_hi:[1,0]
	v_pk_mul_f32 v[14:15], v[14:15], s[2:3] op_sel_hi:[1,0]
	v_exp_f32_e32 v12, v12
	v_exp_f32_e32 v14, v14
	v_exp_f32_e32 v15, v15
	v_exp_f32_e32 v13, v13
	v_pk_add_f32 v[10:11], v[110:111], 1.0 op_sel_hi:[1,0]
	v_pk_add_f32 v[8:9], v[8:9], 1.0 op_sel_hi:[1,0]
	v_rcp_f32_e32 v10, v10
	v_rcp_f32_e32 v11, v11
	v_rcp_f32_e32 v8, v8
	v_rcp_f32_e32 v9, v9
	v_pk_add_f32 v[14:15], v[14:15], 1.0 op_sel_hi:[1,0]
	v_pk_add_f32 v[12:13], v[12:13], 1.0 op_sel_hi:[1,0]
	v_rcp_f32_e32 v14, v14
	v_rcp_f32_e32 v12, v12
	v_rcp_f32_e32 v13, v13
	v_rcp_f32_e32 v15, v15
	v_lshlrev_b32_e32 v174, 16, v150
	v_and_b32_e32 v175, 0xffff0000, v150
	v_lshlrev_b32_e32 v150, 16, v151
	v_and_b32_e32 v151, 0xffff0000, v151
	v_lshlrev_b32_e32 v178, 16, v154
	v_and_b32_e32 v179, 0xffff0000, v154
	v_lshlrev_b32_e32 v154, 16, v155
	v_and_b32_e32 v155, 0xffff0000, v155
	v_pk_fma_f32 v[100:101], v[8:9], v[150:151], v[154:155]
	v_pk_fma_f32 v[110:111], v[10:11], v[174:175], v[178:179]
	v_lshlrev_b32_e32 v176, 16, v152
	v_and_b32_e32 v177, 0xffff0000, v152
	v_lshlrev_b32_e32 v152, 16, v153
	v_and_b32_e32 v153, 0xffff0000, v153
	v_lshlrev_b32_e32 v180, 16, v156
	v_and_b32_e32 v181, 0xffff0000, v156
	v_lshlrev_b32_e32 v156, 16, v157
	v_and_b32_e32 v157, 0xffff0000, v157
	v_mul_f32_e32 v8, v111, v111
	v_mul_f32_e32 v9, v101, v101
	v_pk_fma_f32 v[98:99], v[12:13], v[152:153], v[156:157]
	v_pk_fma_f32 v[112:113], v[14:15], v[176:177], v[180:181]
	v_fmac_f32_e32 v8, v110, v110
	v_fmac_f32_e32 v9, v100, v100
	v_add_f32_e32 v8, v8, v9
	v_mul_f32_e32 v9, v113, v113
	v_mul_f32_e32 v10, v99, v99
	v_fmac_f32_e32 v9, v112, v112
	v_fmac_f32_e32 v10, v98, v98
	v_add_f32_e32 v9, v9, v10
	v_add_f32_e32 v8, v8, v9
	v_add_f32_e32 v7, v7, v8
	ds_bpermute_b32 v8, v4, v7
	s_waitcnt lgkmcnt(0)
	v_add_f32_e32 v7, v7, v8
	ds_bpermute_b32 v8, v6, v7
	s_and_saveexec_b64 s[2:3], vcc
	s_cbranch_execz .LBB0_1490
	s_waitcnt lgkmcnt(0)
	v_add_f32_e32 v7, v7, v8
	ds_write_b32 v5, v7 offset:768
.LBB0_1490:
	s_or_b64 exec, exec, s[2:3]
	s_waitcnt lgkmcnt(0)
	s_waitcnt vmcnt(8)
	v_mov_b64_e32 v[8:9], v[200:201]
	v_mov_b64_e32 v[10:11], v[202:203]
	v_mov_b64_e32 v[12:13], v[204:205]
	v_mov_b64_e32 v[14:15], v[206:207]
	v_mov_b64_e32 v[150:151], v[208:209]
	v_mov_b64_e32 v[152:153], v[210:211]
	v_mov_b64_e32 v[154:155], v[212:213]
	v_mov_b64_e32 v[156:157], v[214:215]
	v_lshl_add_u64 v[254:255], v[254:255], 0, v[250:251]
	v_lshl_add_u64 v[196:197], v[196:197], 0, v[250:251]
	global_load_dwordx4 v[200:203], v[254:255], off
	global_load_dwordx4 v[204:207], v[196:197], off
	global_load_dwordx4 v[208:211], v[254:255], off offset:256
	global_load_dwordx4 v[212:215], v[196:197], off offset:256
	s_mov_b32 s2, 0xbfb8aa3b
	v_pk_mul_f32 v[16:17], v[96:97], s[6:7] op_sel_hi:[1,0]
	v_pk_mul_f32 v[94:95], v[94:95], s[6:7] op_sel_hi:[1,0]
	v_pk_mul_f32 v[92:93], v[92:93], s[6:7] op_sel_hi:[1,0]
	v_pk_mul_f32 v[90:91], v[90:91], s[6:7] op_sel_hi:[1,0]
	v_pk_mul_f32 v[96:97], v[88:89], s[6:7] op_sel_hi:[1,0]
	v_pk_mul_f32 v[86:87], v[86:87], s[6:7] op_sel_hi:[1,0]
	v_pk_mul_f32 v[88:89], v[94:95], s[2:3] op_sel_hi:[1,0]
	v_pk_mul_f32 v[16:17], v[16:17], s[2:3] op_sel_hi:[1,0]
	v_pk_mul_f32 v[90:91], v[90:91], s[2:3] op_sel_hi:[1,0]
	v_pk_mul_f32 v[92:93], v[92:93], s[2:3] op_sel_hi:[1,0]
	v_pk_mul_f32 v[94:95], v[86:87], s[2:3] op_sel_hi:[1,0]
	v_exp_f32_e32 v86, v88
	v_exp_f32_e32 v87, v89
	v_exp_f32_e32 v16, v16
	v_exp_f32_e32 v17, v17
	v_exp_f32_e32 v88, v90
	v_exp_f32_e32 v89, v91
	v_exp_f32_e32 v90, v92
	v_exp_f32_e32 v91, v93
	v_pk_add_f32 v[86:87], v[86:87], 1.0 op_sel_hi:[1,0]
	v_pk_add_f32 v[16:17], v[16:17], 1.0 op_sel_hi:[1,0]
	v_pk_add_f32 v[88:89], v[88:89], 1.0 op_sel_hi:[1,0]
	v_pk_add_f32 v[90:91], v[90:91], 1.0 op_sel_hi:[1,0]
	v_rcp_f32_e32 v86, v86
	v_rcp_f32_e32 v87, v87
	v_rcp_f32_e32 v16, v16
	v_rcp_f32_e32 v17, v17
	v_rcp_f32_e32 v88, v88
	v_rcp_f32_e32 v89, v89
	v_rcp_f32_e32 v158, v90
	v_rcp_f32_e32 v159, v91
	v_add_u32_e32 v19, 0x80, v189
	v_lshlrev_b32_e32 v170, 16, v12
	v_lshlrev_b32_e32 v92, 16, v8
	v_and_b32_e32 v93, 0xffff0000, v8
	v_lshlrev_b32_e32 v8, 16, v9
	v_and_b32_e32 v9, 0xffff0000, v9
	v_lshlrev_b32_e32 v160, 16, v10
	v_and_b32_e32 v161, 0xffff0000, v10
	v_lshlrev_b32_e32 v10, 16, v11
	v_and_b32_e32 v11, 0xffff0000, v11
	v_and_b32_e32 v171, 0xffff0000, v12
	v_lshlrev_b32_e32 v12, 16, v13
	v_and_b32_e32 v13, 0xffff0000, v13
	v_lshlrev_b32_e32 v172, 16, v14
	v_and_b32_e32 v173, 0xffff0000, v14
	v_lshlrev_b32_e32 v14, 16, v15
	v_and_b32_e32 v15, 0xffff0000, v15
	v_pk_fma_f32 v[90:91], v[16:17], v[8:9], v[12:13]
	v_pk_fma_f32 v[92:93], v[86:87], v[92:93], v[170:171]
	v_pk_fma_f32 v[86:87], v[158:159], v[10:11], v[14:15]
	v_pk_fma_f32 v[88:89], v[88:89], v[160:161], v[172:173]
	v_mul_f32_e32 v7, v93, v93
	v_mul_f32_e32 v8, v91, v91
	v_mul_f32_e32 v9, v89, v89
	v_mul_f32_e32 v10, v87, v87
	v_fmac_f32_e32 v7, v92, v92
	v_fmac_f32_e32 v8, v90, v90
	v_fmac_f32_e32 v9, v88, v88
	v_fmac_f32_e32 v10, v86, v86
	v_add_f32_e32 v7, v7, v8
	v_add_f32_e32 v8, v9, v10
	v_pk_mul_f32 v[10:11], v[96:97], s[2:3] op_sel_hi:[1,0]
	v_add_f32_e32 v7, v7, v8
	v_exp_f32_e32 v8, v94
	v_exp_f32_e32 v9, v95
	v_exp_f32_e32 v10, v10
	v_exp_f32_e32 v11, v11
	v_pk_mul_f32 v[12:13], v[84:85], s[6:7] op_sel_hi:[1,0]
	v_pk_mul_f32 v[14:15], v[82:83], s[6:7] op_sel_hi:[1,0]
	v_pk_mul_f32 v[12:13], v[12:13], s[2:3] op_sel_hi:[1,0]
	v_pk_mul_f32 v[14:15], v[14:15], s[2:3] op_sel_hi:[1,0]
	v_exp_f32_e32 v12, v12
	v_exp_f32_e32 v14, v14
	v_exp_f32_e32 v15, v15
	v_exp_f32_e32 v13, v13
	v_pk_add_f32 v[8:9], v[8:9], 1.0 op_sel_hi:[1,0]
	v_pk_add_f32 v[10:11], v[10:11], 1.0 op_sel_hi:[1,0]
	v_rcp_f32_e32 v8, v8
	v_rcp_f32_e32 v9, v9
	v_rcp_f32_e32 v10, v10
	v_rcp_f32_e32 v11, v11
	v_pk_add_f32 v[14:15], v[14:15], 1.0 op_sel_hi:[1,0]
	v_pk_add_f32 v[12:13], v[12:13], 1.0 op_sel_hi:[1,0]
	v_rcp_f32_e32 v14, v14
	v_rcp_f32_e32 v12, v12
	v_rcp_f32_e32 v13, v13
	v_rcp_f32_e32 v15, v15
	v_lshlrev_b32_e32 v174, 16, v150
	v_and_b32_e32 v175, 0xffff0000, v150
	v_lshlrev_b32_e32 v150, 16, v151
	v_and_b32_e32 v151, 0xffff0000, v151
	v_lshlrev_b32_e32 v178, 16, v154
	v_and_b32_e32 v179, 0xffff0000, v154
	v_lshlrev_b32_e32 v154, 16, v155
	v_and_b32_e32 v155, 0xffff0000, v155
	v_pk_fma_f32 v[84:85], v[10:11], v[150:151], v[154:155]
	v_pk_fma_f32 v[94:95], v[8:9], v[174:175], v[178:179]
	v_lshlrev_b32_e32 v176, 16, v152
	v_and_b32_e32 v177, 0xffff0000, v152
	v_lshlrev_b32_e32 v152, 16, v153
	v_and_b32_e32 v153, 0xffff0000, v153
	v_lshlrev_b32_e32 v180, 16, v156
	v_and_b32_e32 v181, 0xffff0000, v156
	v_lshlrev_b32_e32 v156, 16, v157
	v_and_b32_e32 v157, 0xffff0000, v157
	v_mul_f32_e32 v8, v95, v95
	v_mul_f32_e32 v9, v85, v85
	v_pk_fma_f32 v[82:83], v[12:13], v[152:153], v[156:157]
	v_pk_fma_f32 v[96:97], v[14:15], v[176:177], v[180:181]
	v_fmac_f32_e32 v8, v94, v94
	v_fmac_f32_e32 v9, v84, v84
	v_add_f32_e32 v8, v8, v9
	v_mul_f32_e32 v9, v97, v97
	v_mul_f32_e32 v10, v83, v83
	v_fmac_f32_e32 v9, v96, v96
	v_fmac_f32_e32 v10, v82, v82
	v_add_f32_e32 v9, v9, v10
	v_add_f32_e32 v8, v8, v9
	v_add_f32_e32 v7, v7, v8
	ds_bpermute_b32 v8, v4, v7
	s_waitcnt lgkmcnt(0)
	v_add_f32_e32 v7, v7, v8
	ds_bpermute_b32 v8, v6, v7
	s_and_saveexec_b64 s[20:21], vcc
	s_cbranch_execz .LBB0_1492
	v_lshl_add_u32 v9, v19, 4, s5
	s_waitcnt lgkmcnt(0)
	v_add_f32_e32 v7, v7, v8
	ds_write_b32 v9, v7
.LBB0_1492:
	s_or_b64 exec, exec, s[20:21]
	v_add_u32_e32 v150, 0x90, v18
	v_ashrrev_i32_e32 v151, 31, v150
	s_waitcnt lgkmcnt(0)
	s_waitcnt vmcnt(8)
	v_mov_b64_e32 v[8:9], v[216:217]
	v_mov_b64_e32 v[10:11], v[218:219]
	v_mov_b64_e32 v[12:13], v[220:221]
	v_mov_b64_e32 v[14:15], v[222:223]
	v_mov_b64_e32 v[152:153], v[224:225]
	v_mov_b64_e32 v[154:155], v[226:227]
	v_mov_b64_e32 v[156:157], v[228:229]
	v_mov_b64_e32 v[158:159], v[230:231]
	v_pk_mul_f32 v[16:17], v[80:81], s[6:7] op_sel_hi:[1,0]
	v_pk_mul_f32 v[78:79], v[78:79], s[6:7] op_sel_hi:[1,0]
	v_pk_mul_f32 v[76:77], v[76:77], s[6:7] op_sel_hi:[1,0]
	v_pk_mul_f32 v[74:75], v[74:75], s[6:7] op_sel_hi:[1,0]
	v_pk_mul_f32 v[72:73], v[72:73], s[6:7] op_sel_hi:[1,0]
	v_pk_mul_f32 v[78:79], v[78:79], s[2:3] op_sel_hi:[1,0]
	v_pk_mul_f32 v[16:17], v[16:17], s[2:3] op_sel_hi:[1,0]
	v_pk_mul_f32 v[74:75], v[74:75], s[2:3] op_sel_hi:[1,0]
	v_pk_mul_f32 v[76:77], v[76:77], s[2:3] op_sel_hi:[1,0]
	v_pk_mul_f32 v[80:81], v[72:73], s[2:3] op_sel_hi:[1,0]
	v_exp_f32_e32 v72, v78
	v_exp_f32_e32 v73, v79
	v_exp_f32_e32 v16, v16
	v_exp_f32_e32 v17, v17
	v_exp_f32_e32 v74, v74
	v_exp_f32_e32 v75, v75
	v_exp_f32_e32 v76, v76
	v_exp_f32_e32 v77, v77
	v_pk_mul_f32 v[70:71], v[70:71], s[6:7] op_sel_hi:[1,0]
	v_pk_add_f32 v[16:17], v[16:17], 1.0 op_sel_hi:[1,0]
	v_pk_mul_f32 v[70:71], v[70:71], s[2:3] op_sel_hi:[1,0]
	v_rcp_f32_e32 v16, v16
	v_exp_f32_e32 v78, v70
	v_exp_f32_e32 v79, v71
	v_pk_add_f32 v[70:71], v[72:73], 1.0 op_sel_hi:[1,0]
	v_pk_add_f32 v[72:73], v[74:75], 1.0 op_sel_hi:[1,0]
	v_pk_add_f32 v[74:75], v[76:77], 1.0 op_sel_hi:[1,0]
	v_rcp_f32_e32 v70, v70
	v_rcp_f32_e32 v71, v71
	v_rcp_f32_e32 v17, v17
	v_rcp_f32_e32 v72, v72
	v_rcp_f32_e32 v73, v73
	v_rcp_f32_e32 v160, v74
	v_rcp_f32_e32 v161, v75
	v_lshlrev_b32_e32 v172, 16, v12
	v_lshlrev_b32_e32 v76, 16, v8
	v_and_b32_e32 v77, 0xffff0000, v8
	v_lshlrev_b32_e32 v8, 16, v9
	v_and_b32_e32 v9, 0xffff0000, v9
	v_lshlrev_b32_e32 v170, 16, v10
	v_and_b32_e32 v171, 0xffff0000, v10
	v_lshlrev_b32_e32 v10, 16, v11
	v_and_b32_e32 v11, 0xffff0000, v11
	v_and_b32_e32 v173, 0xffff0000, v12
	v_lshlrev_b32_e32 v12, 16, v13
	v_and_b32_e32 v13, 0xffff0000, v13
	v_lshlrev_b32_e32 v174, 16, v14
	v_and_b32_e32 v175, 0xffff0000, v14
	v_lshlrev_b32_e32 v14, 16, v15
	v_and_b32_e32 v15, 0xffff0000, v15
	v_pk_fma_f32 v[74:75], v[16:17], v[8:9], v[12:13]
	v_pk_fma_f32 v[76:77], v[70:71], v[76:77], v[172:173]
	v_pk_fma_f32 v[70:71], v[160:161], v[10:11], v[14:15]
	v_pk_fma_f32 v[72:73], v[72:73], v[170:171], v[174:175]
	v_mul_f32_e32 v7, v77, v77
	v_mul_f32_e32 v8, v75, v75
	v_mul_f32_e32 v9, v73, v73
	v_mul_f32_e32 v10, v71, v71
	v_fmac_f32_e32 v7, v76, v76
	v_fmac_f32_e32 v8, v74, v74
	v_fmac_f32_e32 v9, v72, v72
	v_fmac_f32_e32 v10, v70, v70
	v_add_f32_e32 v7, v7, v8
	v_add_f32_e32 v8, v9, v10
	v_add_f32_e32 v7, v7, v8
	v_exp_f32_e32 v8, v80
	v_exp_f32_e32 v9, v81
	v_pk_mul_f32 v[12:13], v[68:69], s[6:7] op_sel_hi:[1,0]
	v_pk_mul_f32 v[14:15], v[66:67], s[6:7] op_sel_hi:[1,0]
	v_pk_mul_f32 v[12:13], v[12:13], s[2:3] op_sel_hi:[1,0]
	v_pk_mul_f32 v[14:15], v[14:15], s[2:3] op_sel_hi:[1,0]
	v_exp_f32_e32 v12, v12
	v_exp_f32_e32 v14, v14
	v_exp_f32_e32 v15, v15
	v_exp_f32_e32 v13, v13
	v_pk_add_f32 v[10:11], v[78:79], 1.0 op_sel_hi:[1,0]
	v_pk_add_f32 v[8:9], v[8:9], 1.0 op_sel_hi:[1,0]
	v_rcp_f32_e32 v10, v10
	v_rcp_f32_e32 v11, v11
	v_rcp_f32_e32 v8, v8
	v_rcp_f32_e32 v9, v9
	v_pk_add_f32 v[14:15], v[14:15], 1.0 op_sel_hi:[1,0]
	v_pk_add_f32 v[12:13], v[12:13], 1.0 op_sel_hi:[1,0]
	v_rcp_f32_e32 v14, v14
	v_rcp_f32_e32 v12, v12
	v_rcp_f32_e32 v13, v13
	v_rcp_f32_e32 v15, v15
	v_lshlrev_b32_e32 v176, 16, v152
	v_and_b32_e32 v177, 0xffff0000, v152
	v_lshlrev_b32_e32 v152, 16, v153
	v_and_b32_e32 v153, 0xffff0000, v153
	v_lshlrev_b32_e32 v180, 16, v156
	v_and_b32_e32 v181, 0xffff0000, v156
	v_lshlrev_b32_e32 v156, 16, v157
	v_and_b32_e32 v157, 0xffff0000, v157
	v_pk_fma_f32 v[68:69], v[8:9], v[152:153], v[156:157]
	v_pk_fma_f32 v[78:79], v[10:11], v[176:177], v[180:181]
	v_lshlrev_b32_e32 v178, 16, v154
	v_and_b32_e32 v179, 0xffff0000, v154
	v_lshlrev_b32_e32 v154, 16, v155
	v_and_b32_e32 v155, 0xffff0000, v155
	v_lshlrev_b32_e32 v190, 16, v158
	v_and_b32_e32 v191, 0xffff0000, v158
	v_lshlrev_b32_e32 v158, 16, v159
	v_and_b32_e32 v159, 0xffff0000, v159
	v_mul_f32_e32 v8, v79, v79
	v_mul_f32_e32 v9, v69, v69
	v_pk_fma_f32 v[66:67], v[12:13], v[154:155], v[158:159]
	v_pk_fma_f32 v[80:81], v[14:15], v[178:179], v[190:191]
	v_fmac_f32_e32 v8, v78, v78
	v_fmac_f32_e32 v9, v68, v68
	v_add_f32_e32 v8, v8, v9
	v_mul_f32_e32 v9, v81, v81
	v_mul_f32_e32 v10, v67, v67
	v_fmac_f32_e32 v9, v80, v80
	v_fmac_f32_e32 v10, v66, v66
	v_add_f32_e32 v9, v9, v10
	v_add_f32_e32 v8, v8, v9
	v_add_f32_e32 v7, v7, v8
	ds_bpermute_b32 v8, v4, v7
	s_waitcnt lgkmcnt(0)
	v_add_f32_e32 v7, v7, v8
	ds_bpermute_b32 v8, v6, v7
	s_and_saveexec_b64 s[2:3], vcc
	s_cbranch_execz .LBB0_1494
	s_waitcnt lgkmcnt(0)
	v_add_f32_e32 v7, v7, v8
	ds_write_b32 v5, v7 offset:2304
.LBB0_1494:
	s_or_b64 exec, exec, s[2:3]
	v_add_u32_e32 v152, 0xa0, v18
	v_ashrrev_i32_e32 v153, 31, v152
	s_waitcnt lgkmcnt(0)
	s_waitcnt vmcnt(4)
	v_mov_b64_e32 v[8:9], v[232:233]
	v_mov_b64_e32 v[10:11], v[234:235]
	v_mov_b64_e32 v[12:13], v[236:237]
	v_mov_b64_e32 v[14:15], v[238:239]
	v_mov_b64_e32 v[154:155], v[240:241]
	v_mov_b64_e32 v[156:157], v[242:243]
	v_mov_b64_e32 v[158:159], v[244:245]
	v_mov_b64_e32 v[160:161], v[246:247]
	s_mov_b32 s2, 0xbfb8aa3b
	v_pk_mul_f32 v[16:17], v[64:65], s[6:7] op_sel_hi:[1,0]
	v_pk_mul_f32 v[62:63], v[62:63], s[6:7] op_sel_hi:[1,0]
	v_pk_mul_f32 v[60:61], v[60:61], s[6:7] op_sel_hi:[1,0]
	v_pk_mul_f32 v[58:59], v[58:59], s[6:7] op_sel_hi:[1,0]
	v_pk_mul_f32 v[64:65], v[56:57], s[6:7] op_sel_hi:[1,0]
	v_pk_mul_f32 v[54:55], v[54:55], s[6:7] op_sel_hi:[1,0]
	v_pk_mul_f32 v[56:57], v[62:63], s[2:3] op_sel_hi:[1,0]
	v_pk_mul_f32 v[16:17], v[16:17], s[2:3] op_sel_hi:[1,0]
	v_pk_mul_f32 v[58:59], v[58:59], s[2:3] op_sel_hi:[1,0]
	v_pk_mul_f32 v[60:61], v[60:61], s[2:3] op_sel_hi:[1,0]
	v_pk_mul_f32 v[62:63], v[54:55], s[2:3] op_sel_hi:[1,0]
	v_exp_f32_e32 v54, v56
	v_exp_f32_e32 v55, v57
	v_exp_f32_e32 v16, v16
	v_exp_f32_e32 v17, v17
	v_exp_f32_e32 v56, v58
	v_exp_f32_e32 v57, v59
	v_exp_f32_e32 v58, v60
	v_exp_f32_e32 v59, v61
	v_pk_add_f32 v[54:55], v[54:55], 1.0 op_sel_hi:[1,0]
	v_pk_add_f32 v[16:17], v[16:17], 1.0 op_sel_hi:[1,0]
	v_pk_add_f32 v[56:57], v[56:57], 1.0 op_sel_hi:[1,0]
	v_pk_add_f32 v[58:59], v[58:59], 1.0 op_sel_hi:[1,0]
	v_rcp_f32_e32 v54, v54
	v_rcp_f32_e32 v55, v55
	v_rcp_f32_e32 v16, v16
	v_rcp_f32_e32 v17, v17
	v_rcp_f32_e32 v56, v56
	v_rcp_f32_e32 v57, v57
	v_rcp_f32_e32 v170, v58
	v_rcp_f32_e32 v171, v59
	v_exp_f32_e32 v62, v62
	v_exp_f32_e32 v63, v63
	v_lshlrev_b32_e32 v174, 16, v12
	v_lshlrev_b32_e32 v60, 16, v8
	v_and_b32_e32 v61, 0xffff0000, v8
	v_lshlrev_b32_e32 v8, 16, v9
	v_and_b32_e32 v9, 0xffff0000, v9
	v_lshlrev_b32_e32 v172, 16, v10
	v_and_b32_e32 v173, 0xffff0000, v10
	v_lshlrev_b32_e32 v10, 16, v11
	v_and_b32_e32 v11, 0xffff0000, v11
	v_and_b32_e32 v175, 0xffff0000, v12
	v_lshlrev_b32_e32 v12, 16, v13
	v_and_b32_e32 v13, 0xffff0000, v13
	v_lshlrev_b32_e32 v176, 16, v14
	v_and_b32_e32 v177, 0xffff0000, v14
	v_lshlrev_b32_e32 v14, 16, v15
	v_and_b32_e32 v15, 0xffff0000, v15
	v_pk_fma_f32 v[58:59], v[16:17], v[8:9], v[12:13]
	v_pk_fma_f32 v[60:61], v[54:55], v[60:61], v[174:175]
	v_pk_fma_f32 v[54:55], v[170:171], v[10:11], v[14:15]
	v_pk_fma_f32 v[56:57], v[56:57], v[172:173], v[176:177]
	v_mul_f32_e32 v7, v61, v61
	v_mul_f32_e32 v8, v59, v59
	v_mul_f32_e32 v9, v57, v57
	v_mul_f32_e32 v10, v55, v55
	v_fmac_f32_e32 v7, v60, v60
	v_fmac_f32_e32 v8, v58, v58
	v_fmac_f32_e32 v9, v56, v56
	v_fmac_f32_e32 v10, v54, v54
	v_add_f32_e32 v7, v7, v8
	v_add_f32_e32 v8, v9, v10
	v_add_f32_e32 v7, v7, v8
	v_pk_mul_f32 v[8:9], v[64:65], s[2:3] op_sel_hi:[1,0]
	v_pk_mul_f32 v[12:13], v[52:53], s[6:7] op_sel_hi:[1,0]
	v_exp_f32_e32 v8, v8
	v_exp_f32_e32 v9, v9
	v_pk_mul_f32 v[14:15], v[50:51], s[6:7] op_sel_hi:[1,0]
	v_pk_mul_f32 v[12:13], v[12:13], s[2:3] op_sel_hi:[1,0]
	v_pk_mul_f32 v[14:15], v[14:15], s[2:3] op_sel_hi:[1,0]
	v_exp_f32_e32 v12, v12
	v_exp_f32_e32 v14, v14
	v_exp_f32_e32 v15, v15
	v_exp_f32_e32 v13, v13
	v_pk_add_f32 v[10:11], v[62:63], 1.0 op_sel_hi:[1,0]
	v_pk_add_f32 v[8:9], v[8:9], 1.0 op_sel_hi:[1,0]
	v_rcp_f32_e32 v10, v10
	v_rcp_f32_e32 v11, v11
	v_rcp_f32_e32 v8, v8
	v_rcp_f32_e32 v9, v9
	v_pk_add_f32 v[14:15], v[14:15], 1.0 op_sel_hi:[1,0]
	v_pk_add_f32 v[12:13], v[12:13], 1.0 op_sel_hi:[1,0]
	v_rcp_f32_e32 v14, v14
	v_rcp_f32_e32 v12, v12
	v_rcp_f32_e32 v13, v13
	v_rcp_f32_e32 v15, v15
	v_lshlrev_b32_e32 v178, 16, v154
	v_and_b32_e32 v179, 0xffff0000, v154
	v_lshlrev_b32_e32 v154, 16, v155
	v_and_b32_e32 v155, 0xffff0000, v155
	v_lshlrev_b32_e32 v190, 16, v158
	v_and_b32_e32 v191, 0xffff0000, v158
	v_lshlrev_b32_e32 v158, 16, v159
	v_and_b32_e32 v159, 0xffff0000, v159
	v_pk_fma_f32 v[52:53], v[8:9], v[154:155], v[158:159]
	v_pk_fma_f32 v[62:63], v[10:11], v[178:179], v[190:191]
	v_lshlrev_b32_e32 v180, 16, v156
	v_and_b32_e32 v181, 0xffff0000, v156
	v_lshlrev_b32_e32 v156, 16, v157
	v_and_b32_e32 v157, 0xffff0000, v157
	v_lshlrev_b32_e32 v192, 16, v160
	v_and_b32_e32 v193, 0xffff0000, v160
	v_lshlrev_b32_e32 v160, 16, v161
	v_and_b32_e32 v161, 0xffff0000, v161
	v_mul_f32_e32 v8, v63, v63
	v_mul_f32_e32 v9, v53, v53
	v_pk_fma_f32 v[50:51], v[12:13], v[156:157], v[160:161]
	v_pk_fma_f32 v[64:65], v[14:15], v[180:181], v[192:193]
	v_fmac_f32_e32 v8, v62, v62
	v_fmac_f32_e32 v9, v52, v52
	v_add_f32_e32 v8, v8, v9
	v_mul_f32_e32 v9, v65, v65
	v_mul_f32_e32 v10, v51, v51
	v_fmac_f32_e32 v9, v64, v64
	v_fmac_f32_e32 v10, v50, v50
	v_add_f32_e32 v9, v9, v10
	v_add_f32_e32 v8, v8, v9
	v_add_f32_e32 v7, v7, v8
	ds_bpermute_b32 v8, v4, v7
	s_waitcnt lgkmcnt(0)
	v_add_f32_e32 v7, v7, v8
	ds_bpermute_b32 v8, v6, v7
	s_and_saveexec_b64 s[20:21], vcc
	s_cbranch_execz .LBB0_1496
	s_waitcnt lgkmcnt(0)
	v_add_f32_e32 v7, v7, v8
	ds_write_b32 v5, v7 offset:2560
.LBB0_1496:
	s_or_b64 exec, exec, s[20:21]
	v_add_u32_e32 v154, 0xb0, v18
	v_ashrrev_i32_e32 v155, 31, v154
	s_waitcnt lgkmcnt(0)
	s_waitcnt vmcnt(0)
	v_mov_b64_e32 v[8:9], v[200:201]
	v_mov_b64_e32 v[10:11], v[202:203]
	v_mov_b64_e32 v[12:13], v[204:205]
	v_mov_b64_e32 v[14:15], v[206:207]
	v_mov_b64_e32 v[156:157], v[208:209]
	v_mov_b64_e32 v[158:159], v[210:211]
	v_mov_b64_e32 v[170:171], v[212:213]
	v_mov_b64_e32 v[172:173], v[214:215]
	v_pk_mul_f32 v[16:17], v[48:49], s[6:7] op_sel_hi:[1,0]
	v_pk_mul_f32 v[46:47], v[46:47], s[6:7] op_sel_hi:[1,0]
	v_pk_mul_f32 v[44:45], v[44:45], s[6:7] op_sel_hi:[1,0]
	v_pk_mul_f32 v[42:43], v[42:43], s[6:7] op_sel_hi:[1,0]
	v_pk_mul_f32 v[40:41], v[40:41], s[6:7] op_sel_hi:[1,0]
	v_pk_mul_f32 v[46:47], v[46:47], s[2:3] op_sel_hi:[1,0]
	v_pk_mul_f32 v[16:17], v[16:17], s[2:3] op_sel_hi:[1,0]
	v_pk_mul_f32 v[42:43], v[42:43], s[2:3] op_sel_hi:[1,0]
	v_pk_mul_f32 v[44:45], v[44:45], s[2:3] op_sel_hi:[1,0]
	v_pk_mul_f32 v[48:49], v[40:41], s[2:3] op_sel_hi:[1,0]
	v_exp_f32_e32 v40, v46
	v_exp_f32_e32 v41, v47
	v_exp_f32_e32 v16, v16
	v_exp_f32_e32 v17, v17
	v_exp_f32_e32 v42, v42
	v_exp_f32_e32 v43, v43
	v_exp_f32_e32 v44, v44
	v_exp_f32_e32 v45, v45
	v_pk_mul_f32 v[38:39], v[38:39], s[6:7] op_sel_hi:[1,0]
	v_pk_add_f32 v[16:17], v[16:17], 1.0 op_sel_hi:[1,0]
	v_pk_mul_f32 v[38:39], v[38:39], s[2:3] op_sel_hi:[1,0]
	v_rcp_f32_e32 v16, v16
	v_exp_f32_e32 v46, v38
	v_exp_f32_e32 v47, v39
	v_pk_add_f32 v[38:39], v[40:41], 1.0 op_sel_hi:[1,0]
	v_pk_add_f32 v[40:41], v[42:43], 1.0 op_sel_hi:[1,0]
	v_pk_add_f32 v[42:43], v[44:45], 1.0 op_sel_hi:[1,0]
	v_rcp_f32_e32 v38, v38
	v_rcp_f32_e32 v39, v39
	v_rcp_f32_e32 v17, v17
	v_rcp_f32_e32 v40, v40
	v_rcp_f32_e32 v41, v41
	v_rcp_f32_e32 v160, v42
	v_rcp_f32_e32 v161, v43
	v_lshlrev_b32_e32 v176, 16, v12
	v_lshlrev_b32_e32 v44, 16, v8
	v_and_b32_e32 v45, 0xffff0000, v8
	v_lshlrev_b32_e32 v8, 16, v9
	v_and_b32_e32 v9, 0xffff0000, v9
	v_lshlrev_b32_e32 v174, 16, v10
	v_and_b32_e32 v175, 0xffff0000, v10
	v_lshlrev_b32_e32 v10, 16, v11
	v_and_b32_e32 v11, 0xffff0000, v11
	v_and_b32_e32 v177, 0xffff0000, v12
	v_lshlrev_b32_e32 v12, 16, v13
	v_and_b32_e32 v13, 0xffff0000, v13
	v_lshlrev_b32_e32 v178, 16, v14
	v_and_b32_e32 v179, 0xffff0000, v14
	v_lshlrev_b32_e32 v14, 16, v15
	v_and_b32_e32 v15, 0xffff0000, v15
	v_pk_fma_f32 v[42:43], v[16:17], v[8:9], v[12:13]
	v_pk_fma_f32 v[44:45], v[38:39], v[44:45], v[176:177]
	v_pk_fma_f32 v[38:39], v[160:161], v[10:11], v[14:15]
	v_pk_fma_f32 v[40:41], v[40:41], v[174:175], v[178:179]
	v_mul_f32_e32 v7, v45, v45
	v_mul_f32_e32 v8, v43, v43
	v_mul_f32_e32 v9, v41, v41
	v_mul_f32_e32 v10, v39, v39
	v_fmac_f32_e32 v7, v44, v44
	v_fmac_f32_e32 v8, v42, v42
	v_fmac_f32_e32 v9, v40, v40
	v_fmac_f32_e32 v10, v38, v38
	v_add_f32_e32 v7, v7, v8
	v_add_f32_e32 v8, v9, v10
	v_add_f32_e32 v7, v7, v8
	v_exp_f32_e32 v8, v48
	v_exp_f32_e32 v9, v49
	v_pk_mul_f32 v[12:13], v[36:37], s[6:7] op_sel_hi:[1,0]
	v_pk_mul_f32 v[14:15], v[34:35], s[6:7] op_sel_hi:[1,0]
	v_pk_mul_f32 v[12:13], v[12:13], s[2:3] op_sel_hi:[1,0]
	v_pk_mul_f32 v[14:15], v[14:15], s[2:3] op_sel_hi:[1,0]
	v_exp_f32_e32 v12, v12
	v_exp_f32_e32 v14, v14
	v_exp_f32_e32 v15, v15
	v_exp_f32_e32 v13, v13
	v_pk_add_f32 v[10:11], v[46:47], 1.0 op_sel_hi:[1,0]
	v_pk_add_f32 v[8:9], v[8:9], 1.0 op_sel_hi:[1,0]
	v_rcp_f32_e32 v10, v10
	v_rcp_f32_e32 v11, v11
	v_rcp_f32_e32 v8, v8
	v_rcp_f32_e32 v9, v9
	v_pk_add_f32 v[14:15], v[14:15], 1.0 op_sel_hi:[1,0]
	v_pk_add_f32 v[12:13], v[12:13], 1.0 op_sel_hi:[1,0]
	v_rcp_f32_e32 v14, v14
	v_rcp_f32_e32 v12, v12
	v_rcp_f32_e32 v13, v13
	v_rcp_f32_e32 v15, v15
	v_lshlrev_b32_e32 v180, 16, v156
	v_and_b32_e32 v181, 0xffff0000, v156
	v_lshlrev_b32_e32 v156, 16, v157
	v_and_b32_e32 v157, 0xffff0000, v157
	v_lshlrev_b32_e32 v192, 16, v170
	v_and_b32_e32 v193, 0xffff0000, v170
	v_lshlrev_b32_e32 v170, 16, v171
	v_and_b32_e32 v171, 0xffff0000, v171
	v_pk_fma_f32 v[36:37], v[8:9], v[156:157], v[170:171]
	v_pk_fma_f32 v[46:47], v[10:11], v[180:181], v[192:193]
	v_lshlrev_b32_e32 v190, 16, v158
	v_and_b32_e32 v191, 0xffff0000, v158
	v_lshlrev_b32_e32 v158, 16, v159
	v_and_b32_e32 v159, 0xffff0000, v159
	v_lshlrev_b32_e32 v194, 16, v172
	v_and_b32_e32 v195, 0xffff0000, v172
	v_lshlrev_b32_e32 v172, 16, v173
	v_and_b32_e32 v173, 0xffff0000, v173
	v_mul_f32_e32 v8, v47, v47
	v_mul_f32_e32 v9, v37, v37
	v_pk_fma_f32 v[34:35], v[12:13], v[158:159], v[172:173]
	v_pk_fma_f32 v[48:49], v[14:15], v[190:191], v[194:195]
	v_fmac_f32_e32 v8, v46, v46
	v_fmac_f32_e32 v9, v36, v36
	v_add_f32_e32 v8, v8, v9
	v_mul_f32_e32 v9, v49, v49
	v_mul_f32_e32 v10, v35, v35
	v_fmac_f32_e32 v9, v48, v48
	v_fmac_f32_e32 v10, v34, v34
	v_add_f32_e32 v9, v9, v10
	v_add_f32_e32 v8, v8, v9
	v_add_f32_e32 v7, v7, v8
	ds_bpermute_b32 v4, v4, v7
	s_waitcnt lgkmcnt(0)
	v_add_f32_e32 v4, v7, v4
	ds_bpermute_b32 v6, v6, v4
	s_and_saveexec_b64 s[2:3], vcc
	s_cbranch_execz .LBB0_1498
	s_waitcnt lgkmcnt(0)
	v_add_f32_e32 v4, v4, v6
	ds_write_b32 v5, v4 offset:2816

.LBB0_1533:
	s_lshl_b32 s2, s5, 5
	s_lshl_b32 s1, s0, 8
	s_lshl_b32 s3, s4, 8
	s_or_b32 s2, s3, s2
	v_add_u32_e32 v18, s1, v189
	v_or_b32_e32 v2, s2, v1
	v_ashrrev_i32_e32 v19, 31, v18
	v_ashrrev_i32_e32 v3, 31, v2
	v_lshlrev_b64 v[4:5], 11, v[18:19]
	v_lshl_add_u64 v[20:21], v[4:5], 0, v[2:3]
	v_lshlrev_b64 v[8:9], 1, v[20:21]
	v_lshl_add_u64 v[12:13], s[18:19], 0, v[8:9]
	s_barrier
	global_load_dwordx4 v[4:7], v[12:13], off
	v_lshl_add_u64 v[16:17], s[16:17], 0, v[8:9]
	global_load_dwordx4 v[8:11], v[16:17], off
	s_nop 0
	global_load_dwordx4 v[12:15], v[12:13], off offset:256
	s_nop 0
	global_load_dwordx4 v[30:33], v[16:17], off offset:256
	v_lshlrev_b64 v[254:255], 11, v[18:19]
	v_lshl_add_u64 v[254:255], v[254:255], 0, v[2:3]
	v_lshlrev_b64 v[254:255], 1, v[254:255]
	v_mov_b32_e32 v250, 0x10000
	v_mov_b32_e32 v251, 0
	v_lshl_add_u64 v[196:197], s[16:17], 0, v[254:255]
	v_lshl_add_u64 v[254:255], s[18:19], 0, v[254:255]
	v_lshl_add_u64 v[254:255], v[254:255], 0, v[250:251]
	v_lshl_add_u64 v[196:197], v[196:197], 0, v[250:251]
	global_load_dwordx4 v[200:203], v[254:255], off
	global_load_dwordx4 v[204:207], v[196:197], off
	global_load_dwordx4 v[208:211], v[254:255], off offset:256
	global_load_dwordx4 v[212:215], v[196:197], off offset:256
	v_lshl_add_u64 v[254:255], v[254:255], 0, v[250:251]
	v_lshl_add_u64 v[196:197], v[196:197], 0, v[250:251]
	global_load_dwordx4 v[216:219], v[254:255], off
	global_load_dwordx4 v[220:223], v[196:197], off
	global_load_dwordx4 v[224:227], v[254:255], off offset:256
	global_load_dwordx4 v[228:231], v[196:197], off offset:256
	v_lshl_add_u64 v[254:255], v[254:255], 0, v[250:251]
	v_lshl_add_u64 v[196:197], v[196:197], 0, v[250:251]
	global_load_dwordx4 v[232:235], v[254:255], off
	global_load_dwordx4 v[236:239], v[196:197], off
	global_load_dwordx4 v[240:243], v[254:255], off offset:256
	global_load_dwordx4 v[244:247], v[196:197], off offset:256
	s_mov_b32 s6, 0x3c800000
	s_mov_b32 s2, 0xbfb8aa3b
	v_pk_mul_f32 v[16:17], v[160:161], s[6:7] op_sel_hi:[1,0]
	v_pk_mul_f32 v[22:23], v[158:159], s[6:7] op_sel_hi:[1,0]
	v_pk_mul_f32 v[24:25], v[156:157], s[6:7] op_sel_hi:[1,0]
	v_pk_mul_f32 v[26:27], v[154:155], s[6:7] op_sel_hi:[1,0]
	v_pk_mul_f32 v[22:23], v[22:23], s[2:3] op_sel_hi:[1,0]
	v_pk_mul_f32 v[16:17], v[16:17], s[2:3] op_sel_hi:[1,0]
	v_pk_mul_f32 v[26:27], v[26:27], s[2:3] op_sel_hi:[1,0]
	v_pk_mul_f32 v[24:25], v[24:25], s[2:3] op_sel_hi:[1,0]
	v_exp_f32_e32 v22, v22
	v_exp_f32_e32 v23, v23
	v_exp_f32_e32 v16, v16
	v_exp_f32_e32 v17, v17
	v_exp_f32_e32 v26, v26
	v_exp_f32_e32 v27, v27
	v_exp_f32_e32 v24, v24
	v_exp_f32_e32 v25, v25
	v_pk_add_f32 v[22:23], v[22:23], 1.0 op_sel_hi:[1,0]
	v_pk_add_f32 v[16:17], v[16:17], 1.0 op_sel_hi:[1,0]
	v_pk_add_f32 v[26:27], v[26:27], 1.0 op_sel_hi:[1,0]
	v_pk_add_f32 v[24:25], v[24:25], 1.0 op_sel_hi:[1,0]
	v_mbcnt_lo_u32_b32 v1, -1, 0
	v_rcp_f32_e32 v22, v22
	v_rcp_f32_e32 v23, v23
	v_rcp_f32_e32 v16, v16
	v_rcp_f32_e32 v17, v17
	v_rcp_f32_e32 v26, v26
	v_rcp_f32_e32 v27, v27
	v_rcp_f32_e32 v154, v24
	v_rcp_f32_e32 v155, v25
	v_mbcnt_hi_u32_b32 v166, -1, v1
	v_and_b32_e32 v28, 64, v166
	v_add_u32_e32 v167, 64, v28
	v_pk_mul_f32 v[146:147], v[146:147], s[6:7] op_sel_hi:[1,0]
	v_xor_b32_e32 v1, 16, v166
	v_pk_mul_f32 v[146:147], v[146:147], s[2:3] op_sel_hi:[1,0]
	v_cmp_lt_i32_e32 vcc, v1, v167
	v_exp_f32_e32 v146, v146
	v_exp_f32_e32 v147, v147
	v_cndmask_b32_e32 v1, v166, v1, vcc
	v_lshlrev_b32_e32 v1, 2, v1
	v_pk_add_f32 v[146:147], v[146:147], 1.0 op_sel_hi:[1,0]
	s_waitcnt vmcnt(12)
	v_lshlrev_b32_e32 v158, 16, v8
	v_lshlrev_b32_e32 v28, 16, v4
	v_and_b32_e32 v29, 0xffff0000, v4
	v_lshlrev_b32_e32 v4, 16, v5
	v_and_b32_e32 v5, 0xffff0000, v5
	v_lshlrev_b32_e32 v156, 16, v6
	v_and_b32_e32 v157, 0xffff0000, v6
	v_lshlrev_b32_e32 v6, 16, v7
	v_and_b32_e32 v7, 0xffff0000, v7
	v_and_b32_e32 v159, 0xffff0000, v8
	v_lshlrev_b32_e32 v8, 16, v9
	v_and_b32_e32 v9, 0xffff0000, v9
	v_lshlrev_b32_e32 v160, 16, v10
	v_and_b32_e32 v161, 0xffff0000, v10
	v_lshlrev_b32_e32 v10, 16, v11
	v_and_b32_e32 v11, 0xffff0000, v11
	v_pk_fma_f32 v[24:25], v[16:17], v[4:5], v[8:9]
	v_pk_fma_f32 v[28:29], v[22:23], v[28:29], v[158:159]
	v_pk_fma_f32 v[22:23], v[154:155], v[6:7], v[10:11]
	v_pk_fma_f32 v[26:27], v[26:27], v[156:157], v[160:161]
	v_mul_f32_e32 v4, v29, v29
	v_mul_f32_e32 v5, v25, v25
	v_mul_f32_e32 v6, v27, v27
	v_mul_f32_e32 v7, v23, v23
	v_fmac_f32_e32 v4, v28, v28
	v_fmac_f32_e32 v5, v24, v24
	v_fmac_f32_e32 v6, v26, v26
	v_fmac_f32_e32 v7, v22, v22
	v_add_f32_e32 v4, v4, v5
	v_add_f32_e32 v5, v6, v7
	v_lshlrev_b32_e32 v6, 16, v30
	v_and_b32_e32 v7, 0xffff0000, v30
	v_lshlrev_b32_e32 v8, 16, v31
	v_and_b32_e32 v9, 0xffff0000, v31
	v_pk_mul_f32 v[30:31], v[150:151], s[6:7] op_sel_hi:[1,0]
	v_pk_mul_f32 v[16:17], v[152:153], s[6:7] op_sel_hi:[1,0]
	v_pk_mul_f32 v[30:31], v[30:31], s[2:3] op_sel_hi:[1,0]
	v_lshlrev_b32_e32 v164, 16, v14
	v_exp_f32_e32 v30, v30
	v_exp_f32_e32 v31, v31
	v_and_b32_e32 v165, 0xffff0000, v14
	v_add_f32_e32 v154, v4, v5
	v_lshlrev_b32_e32 v4, 16, v15
	v_pk_add_f32 v[30:31], v[30:31], 1.0 op_sel_hi:[1,0]
	v_and_b32_e32 v5, 0xffff0000, v15
	v_lshlrev_b32_e32 v10, 16, v32
	v_and_b32_e32 v11, 0xffff0000, v32
	v_lshlrev_b32_e32 v14, 16, v33
	v_and_b32_e32 v15, 0xffff0000, v33
	v_pk_mul_f32 v[16:17], v[16:17], s[2:3] op_sel_hi:[1,0]
	v_rcp_f32_e32 v32, v30
	v_rcp_f32_e32 v33, v31
	v_pk_mul_f32 v[30:31], v[148:149], s[6:7] op_sel_hi:[1,0]
	v_exp_f32_e32 v16, v16
	v_exp_f32_e32 v17, v17
	v_pk_mul_f32 v[30:31], v[30:31], s[2:3] op_sel_hi:[1,0]
	v_rcp_f32_e32 v148, v146
	v_exp_f32_e32 v30, v30
	v_exp_f32_e32 v31, v31
	v_pk_add_f32 v[16:17], v[16:17], 1.0 op_sel_hi:[1,0]
	v_rcp_f32_e32 v149, v147
	v_rcp_f32_e32 v16, v16
	v_rcp_f32_e32 v17, v17
	v_pk_add_f32 v[30:31], v[30:31], 1.0 op_sel_hi:[1,0]
	v_lshlrev_b32_e32 v162, 16, v12
	v_rcp_f32_e32 v150, v30
	v_rcp_f32_e32 v151, v31
	v_and_b32_e32 v163, 0xffff0000, v12
	v_lshlrev_b32_e32 v12, 16, v13
	v_and_b32_e32 v13, 0xffff0000, v13
	v_pk_fma_f32 v[30:31], v[16:17], v[12:13], v[8:9]
	v_pk_fma_f32 v[32:33], v[32:33], v[162:163], v[6:7]
	v_pk_fma_f32 v[146:147], v[150:151], v[4:5], v[14:15]
	v_mul_f32_e32 v4, v33, v33
	v_mul_f32_e32 v5, v31, v31
	v_pk_fma_f32 v[148:149], v[148:149], v[164:165], v[10:11]
	v_fmac_f32_e32 v4, v32, v32
	v_fmac_f32_e32 v5, v30, v30
	v_add_f32_e32 v4, v4, v5
	v_mul_f32_e32 v5, v149, v149
	v_mul_f32_e32 v6, v147, v147
	v_fmac_f32_e32 v5, v148, v148
	v_fmac_f32_e32 v6, v146, v146
	v_add_f32_e32 v5, v5, v6
	v_add_f32_e32 v4, v4, v5
	v_add_f32_e32 v4, v154, v4
	ds_bpermute_b32 v6, v1, v4
	v_xor_b32_e32 v5, 32, v166
	v_cmp_lt_i32_e32 vcc, v5, v167
	s_lshl_b32 s3, s5, 2
	s_add_i32 s5, s3, 0
	v_cndmask_b32_e32 v5, v166, v5, vcc
	v_lshlrev_b32_e32 v5, 2, v5
	s_waitcnt lgkmcnt(0)
	v_add_f32_e32 v6, v4, v6
	ds_bpermute_b32 v7, v5, v6
	v_cmp_gt_u32_e32 vcc, 16, v198
	v_lshl_add_u32 v4, v189, 4, s5
	s_and_saveexec_b64 s[20:21], vcc
	s_cbranch_execz .LBB0_1535
	s_waitcnt lgkmcnt(0)
	v_add_f32_e32 v6, v6, v7
	ds_write_b32 v4, v6
.LBB0_1535:
	s_or_b64 exec, exec, s[20:21]
	s_waitcnt lgkmcnt(0)
	s_waitcnt vmcnt(8)
	v_mov_b64_e32 v[6:7], v[200:201]
	v_mov_b64_e32 v[8:9], v[202:203]
	v_mov_b64_e32 v[10:11], v[204:205]
	v_mov_b64_e32 v[12:13], v[206:207]
	v_mov_b64_e32 v[14:15], v[208:209]
	v_mov_b64_e32 v[16:17], v[210:211]
	v_mov_b64_e32 v[150:151], v[212:213]
	v_mov_b64_e32 v[152:153], v[214:215]
	v_lshl_add_u64 v[254:255], v[254:255], 0, v[250:251]
	v_lshl_add_u64 v[196:197], v[196:197], 0, v[250:251]
	v_lshl_add_u64 v[254:255], v[254:255], 0, v[250:251]
	v_lshl_add_u64 v[196:197], v[196:197], 0, v[250:251]
	v_lshl_add_u64 v[254:255], v[254:255], 0, v[250:251]
	v_lshl_add_u64 v[196:197], v[196:197], 0, v[250:251]
	v_lshl_add_u64 v[254:255], v[254:255], 0, v[250:251]
	v_lshl_add_u64 v[196:197], v[196:197], 0, v[250:251]
	v_lshl_add_u64 v[254:255], v[254:255], 0, v[250:251]
	v_lshl_add_u64 v[196:197], v[196:197], 0, v[250:251]
	global_load_dwordx4 v[200:203], v[254:255], off
	global_load_dwordx4 v[204:207], v[196:197], off
	global_load_dwordx4 v[208:211], v[254:255], off offset:256
	global_load_dwordx4 v[212:215], v[196:197], off offset:256
	v_pk_mul_f32 v[144:145], v[144:145], s[6:7] op_sel_hi:[1,0]
	v_pk_mul_f32 v[142:143], v[142:143], s[6:7] op_sel_hi:[1,0]
	v_pk_mul_f32 v[140:141], v[140:141], s[6:7] op_sel_hi:[1,0]
	v_pk_mul_f32 v[138:139], v[138:139], s[6:7] op_sel_hi:[1,0]
	v_pk_mul_f32 v[136:137], v[136:137], s[6:7] op_sel_hi:[1,0]
	v_pk_mul_f32 v[142:143], v[142:143], s[2:3] op_sel_hi:[1,0]
	v_pk_mul_f32 v[144:145], v[144:145], s[2:3] op_sel_hi:[1,0]
	v_pk_mul_f32 v[138:139], v[138:139], s[2:3] op_sel_hi:[1,0]
	v_pk_mul_f32 v[140:141], v[140:141], s[2:3] op_sel_hi:[1,0]
	v_pk_mul_f32 v[154:155], v[136:137], s[2:3] op_sel_hi:[1,0]
	v_exp_f32_e32 v136, v142
	v_exp_f32_e32 v137, v143
	v_exp_f32_e32 v142, v144
	v_exp_f32_e32 v143, v145
	v_exp_f32_e32 v138, v138
	v_exp_f32_e32 v139, v139
	v_exp_f32_e32 v140, v140
	v_exp_f32_e32 v141, v141
	v_pk_mul_f32 v[134:135], v[134:135], s[6:7] op_sel_hi:[1,0]
	v_pk_add_f32 v[138:139], v[138:139], 1.0 op_sel_hi:[1,0]
	v_pk_mul_f32 v[134:135], v[134:135], s[2:3] op_sel_hi:[1,0]
	v_pk_add_f32 v[140:141], v[140:141], 1.0 op_sel_hi:[1,0]
	v_exp_f32_e32 v144, v134
	v_exp_f32_e32 v145, v135
	v_pk_add_f32 v[134:135], v[136:137], 1.0 op_sel_hi:[1,0]
	v_pk_add_f32 v[136:137], v[142:143], 1.0 op_sel_hi:[1,0]
	v_rcp_f32_e32 v134, v134
	v_rcp_f32_e32 v135, v135
	v_rcp_f32_e32 v136, v136
	v_rcp_f32_e32 v137, v137
	v_rcp_f32_e32 v138, v138
	v_rcp_f32_e32 v139, v139
	v_rcp_f32_e32 v142, v140
	v_rcp_f32_e32 v143, v141
	v_lshlrev_b32_e32 v158, 16, v10
	v_lshlrev_b32_e32 v140, 16, v6
	v_and_b32_e32 v141, 0xffff0000, v6
	v_lshlrev_b32_e32 v6, 16, v7
	v_and_b32_e32 v7, 0xffff0000, v7
	v_lshlrev_b32_e32 v156, 16, v8
	v_and_b32_e32 v157, 0xffff0000, v8
	v_lshlrev_b32_e32 v8, 16, v9
	v_and_b32_e32 v9, 0xffff0000, v9
	v_and_b32_e32 v159, 0xffff0000, v10
	v_lshlrev_b32_e32 v10, 16, v11
	v_and_b32_e32 v11, 0xffff0000, v11
	v_lshlrev_b32_e32 v160, 16, v12
	v_and_b32_e32 v161, 0xffff0000, v12
	v_lshlrev_b32_e32 v12, 16, v13
	v_and_b32_e32 v13, 0xffff0000, v13
	v_pk_fma_f32 v[136:137], v[136:137], v[6:7], v[10:11]
	v_pk_fma_f32 v[140:141], v[134:135], v[140:141], v[158:159]
	v_pk_fma_f32 v[134:135], v[142:143], v[8:9], v[12:13]
	v_pk_fma_f32 v[138:139], v[138:139], v[156:157], v[160:161]
	v_mul_f32_e32 v6, v141, v141
	v_mul_f32_e32 v7, v137, v137
	v_mul_f32_e32 v8, v139, v139
	v_mul_f32_e32 v9, v135, v135
	v_fmac_f32_e32 v6, v140, v140
	v_fmac_f32_e32 v7, v136, v136
	v_fmac_f32_e32 v8, v138, v138
	v_fmac_f32_e32 v9, v134, v134
	v_add_f32_e32 v6, v6, v7
	v_add_f32_e32 v7, v8, v9
	v_add_f32_e32 v156, v6, v7
	v_exp_f32_e32 v6, v154
	v_exp_f32_e32 v7, v155
	v_pk_mul_f32 v[10:11], v[132:133], s[6:7] op_sel_hi:[1,0]
	v_pk_mul_f32 v[12:13], v[130:131], s[6:7] op_sel_hi:[1,0]
	v_pk_mul_f32 v[10:11], v[10:11], s[2:3] op_sel_hi:[1,0]
	v_pk_mul_f32 v[12:13], v[12:13], s[2:3] op_sel_hi:[1,0]
	v_exp_f32_e32 v10, v10
	v_exp_f32_e32 v12, v12
	v_exp_f32_e32 v13, v13
	v_exp_f32_e32 v11, v11
	v_pk_add_f32 v[8:9], v[144:145], 1.0 op_sel_hi:[1,0]
	v_pk_add_f32 v[6:7], v[6:7], 1.0 op_sel_hi:[1,0]
	v_rcp_f32_e32 v8, v8
	v_rcp_f32_e32 v9, v9
	v_rcp_f32_e32 v6, v6
	v_rcp_f32_e32 v7, v7
	v_pk_add_f32 v[12:13], v[12:13], 1.0 op_sel_hi:[1,0]
	v_pk_add_f32 v[10:11], v[10:11], 1.0 op_sel_hi:[1,0]
	v_rcp_f32_e32 v12, v12
	v_rcp_f32_e32 v10, v10
	v_rcp_f32_e32 v11, v11
	v_rcp_f32_e32 v13, v13
	v_lshlrev_b32_e32 v162, 16, v14
	v_and_b32_e32 v163, 0xffff0000, v14
	v_lshlrev_b32_e32 v14, 16, v15
	v_and_b32_e32 v15, 0xffff0000, v15
	v_lshlrev_b32_e32 v166, 16, v150
	v_and_b32_e32 v167, 0xffff0000, v150
	v_lshlrev_b32_e32 v150, 16, v151
	v_and_b32_e32 v151, 0xffff0000, v151
	v_pk_fma_f32 v[130:131], v[6:7], v[14:15], v[150:151]
	v_pk_fma_f32 v[132:133], v[8:9], v[162:163], v[166:167]
	v_lshlrev_b32_e32 v164, 16, v16
	v_and_b32_e32 v165, 0xffff0000, v16
	v_lshlrev_b32_e32 v16, 16, v17
	v_and_b32_e32 v17, 0xffff0000, v17
	v_lshlrev_b32_e32 v168, 16, v152
	v_and_b32_e32 v169, 0xffff0000, v152
	v_lshlrev_b32_e32 v152, 16, v153
	v_and_b32_e32 v153, 0xffff0000, v153
	v_mul_f32_e32 v6, v133, v133
	v_mul_f32_e32 v7, v131, v131
	v_pk_fma_f32 v[142:143], v[10:11], v[16:17], v[152:153]
	v_pk_fma_f32 v[144:145], v[12:13], v[164:165], v[168:169]
	v_fmac_f32_e32 v6, v132, v132
	v_fmac_f32_e32 v7, v130, v130
	v_add_f32_e32 v6, v6, v7
	v_mul_f32_e32 v7, v145, v145
	v_mul_f32_e32 v8, v143, v143
	v_fmac_f32_e32 v7, v144, v144
	v_fmac_f32_e32 v8, v142, v142
	v_add_f32_e32 v7, v7, v8
	v_add_f32_e32 v6, v6, v7
	v_add_f32_e32 v6, v156, v6
	ds_bpermute_b32 v7, v1, v6
	s_waitcnt lgkmcnt(0)
	v_add_f32_e32 v6, v6, v7
	ds_bpermute_b32 v7, v5, v6
	s_and_saveexec_b64 s[2:3], vcc
	s_cbranch_execz .LBB0_1537
	s_waitcnt lgkmcnt(0)
	v_add_f32_e32 v6, v6, v7
	ds_write_b32 v4, v6 offset:256
.LBB0_1537:
	s_or_b64 exec, exec, s[2:3]
	s_waitcnt lgkmcnt(0)
	s_waitcnt vmcnt(8)
	v_mov_b64_e32 v[6:7], v[216:217]
	v_mov_b64_e32 v[8:9], v[218:219]
	v_mov_b64_e32 v[10:11], v[220:221]
	v_mov_b64_e32 v[12:13], v[222:223]
	v_mov_b64_e32 v[14:15], v[224:225]
	v_mov_b64_e32 v[16:17], v[226:227]
	v_mov_b64_e32 v[150:151], v[228:229]
	v_mov_b64_e32 v[152:153], v[230:231]
	v_lshl_add_u64 v[254:255], v[254:255], 0, v[250:251]
	v_lshl_add_u64 v[196:197], v[196:197], 0, v[250:251]
	global_load_dwordx4 v[216:219], v[254:255], off
	global_load_dwordx4 v[220:223], v[196:197], off
	global_load_dwordx4 v[224:227], v[254:255], off offset:256
	global_load_dwordx4 v[228:231], v[196:197], off offset:256
	s_mov_b32 s2, 0xbfb8aa3b
	v_pk_mul_f32 v[128:129], v[128:129], s[6:7] op_sel_hi:[1,0]
	v_pk_mul_f32 v[126:127], v[126:127], s[6:7] op_sel_hi:[1,0]
	v_pk_mul_f32 v[124:125], v[124:125], s[6:7] op_sel_hi:[1,0]
	v_pk_mul_f32 v[122:123], v[122:123], s[6:7] op_sel_hi:[1,0]
	v_pk_mul_f32 v[154:155], v[120:121], s[6:7] op_sel_hi:[1,0]
	v_pk_mul_f32 v[118:119], v[118:119], s[6:7] op_sel_hi:[1,0]
	v_pk_mul_f32 v[120:121], v[126:127], s[2:3] op_sel_hi:[1,0]
	v_pk_mul_f32 v[126:127], v[128:129], s[2:3] op_sel_hi:[1,0]
	v_pk_mul_f32 v[122:123], v[122:123], s[2:3] op_sel_hi:[1,0]
	v_pk_mul_f32 v[124:125], v[124:125], s[2:3] op_sel_hi:[1,0]
	v_pk_mul_f32 v[128:129], v[118:119], s[2:3] op_sel_hi:[1,0]
	v_exp_f32_e32 v118, v120
	v_exp_f32_e32 v119, v121
	v_exp_f32_e32 v120, v126
	v_exp_f32_e32 v121, v127
	v_exp_f32_e32 v122, v122
	v_exp_f32_e32 v123, v123
	v_exp_f32_e32 v124, v124
	v_exp_f32_e32 v125, v125
	v_pk_add_f32 v[118:119], v[118:119], 1.0 op_sel_hi:[1,0]
	v_pk_add_f32 v[120:121], v[120:121], 1.0 op_sel_hi:[1,0]
	v_pk_add_f32 v[122:123], v[122:123], 1.0 op_sel_hi:[1,0]
	v_pk_add_f32 v[124:125], v[124:125], 1.0 op_sel_hi:[1,0]
	v_rcp_f32_e32 v118, v118
	v_rcp_f32_e32 v119, v119
	v_rcp_f32_e32 v120, v120
	v_rcp_f32_e32 v121, v121
	v_rcp_f32_e32 v122, v122
	v_rcp_f32_e32 v123, v123
	v_rcp_f32_e32 v156, v124
	v_rcp_f32_e32 v157, v125
	v_exp_f32_e32 v126, v128
	v_exp_f32_e32 v127, v129
	v_lshlrev_b32_e32 v160, 16, v10
	v_lshlrev_b32_e32 v124, 16, v6
	v_and_b32_e32 v125, 0xffff0000, v6
	v_lshlrev_b32_e32 v6, 16, v7
	v_and_b32_e32 v7, 0xffff0000, v7
	v_lshlrev_b32_e32 v158, 16, v8
	v_and_b32_e32 v159, 0xffff0000, v8
	v_lshlrev_b32_e32 v8, 16, v9
	v_and_b32_e32 v9, 0xffff0000, v9
	v_and_b32_e32 v161, 0xffff0000, v10
	v_lshlrev_b32_e32 v10, 16, v11
	v_and_b32_e32 v11, 0xffff0000, v11
	v_lshlrev_b32_e32 v162, 16, v12
	v_and_b32_e32 v163, 0xffff0000, v12
	v_lshlrev_b32_e32 v12, 16, v13
	v_and_b32_e32 v13, 0xffff0000, v13
	v_pk_fma_f32 v[120:121], v[120:121], v[6:7], v[10:11]
	v_pk_fma_f32 v[124:125], v[118:119], v[124:125], v[160:161]
	v_pk_fma_f32 v[118:119], v[156:157], v[8:9], v[12:13]
	v_pk_fma_f32 v[122:123], v[122:123], v[158:159], v[162:163]
	v_mul_f32_e32 v6, v125, v125
	v_mul_f32_e32 v7, v121, v121
	v_mul_f32_e32 v8, v123, v123
	v_mul_f32_e32 v9, v119, v119
	v_fmac_f32_e32 v6, v124, v124
	v_fmac_f32_e32 v7, v120, v120
	v_fmac_f32_e32 v8, v122, v122
	v_fmac_f32_e32 v9, v118, v118
	v_add_f32_e32 v6, v6, v7
	v_add_f32_e32 v7, v8, v9
	v_add_f32_e32 v156, v6, v7
	v_pk_mul_f32 v[6:7], v[154:155], s[2:3] op_sel_hi:[1,0]
	v_pk_mul_f32 v[10:11], v[116:117], s[6:7] op_sel_hi:[1,0]
	v_exp_f32_e32 v6, v6
	v_exp_f32_e32 v7, v7
	v_pk_mul_f32 v[12:13], v[114:115], s[6:7] op_sel_hi:[1,0]
	v_pk_mul_f32 v[10:11], v[10:11], s[2:3] op_sel_hi:[1,0]
	v_pk_mul_f32 v[12:13], v[12:13], s[2:3] op_sel_hi:[1,0]
	v_exp_f32_e32 v10, v10
	v_exp_f32_e32 v12, v12
	v_exp_f32_e32 v13, v13
	v_exp_f32_e32 v11, v11
	v_pk_add_f32 v[8:9], v[126:127], 1.0 op_sel_hi:[1,0]
	v_pk_add_f32 v[6:7], v[6:7], 1.0 op_sel_hi:[1,0]
	v_rcp_f32_e32 v8, v8
	v_rcp_f32_e32 v9, v9
	v_rcp_f32_e32 v6, v6
	v_rcp_f32_e32 v7, v7
	v_pk_add_f32 v[12:13], v[12:13], 1.0 op_sel_hi:[1,0]
	v_pk_add_f32 v[10:11], v[10:11], 1.0 op_sel_hi:[1,0]
	v_rcp_f32_e32 v12, v12
	v_rcp_f32_e32 v10, v10
	v_rcp_f32_e32 v11, v11
	v_rcp_f32_e32 v13, v13
	v_lshlrev_b32_e32 v164, 16, v14
	v_and_b32_e32 v165, 0xffff0000, v14
	v_lshlrev_b32_e32 v14, 16, v15
	v_and_b32_e32 v15, 0xffff0000, v15
	v_lshlrev_b32_e32 v168, 16, v150
	v_and_b32_e32 v169, 0xffff0000, v150
	v_lshlrev_b32_e32 v150, 16, v151
	v_and_b32_e32 v151, 0xffff0000, v151
	v_pk_fma_f32 v[114:115], v[6:7], v[14:15], v[150:151]
	v_pk_fma_f32 v[116:117], v[8:9], v[164:165], v[168:169]
	v_lshlrev_b32_e32 v166, 16, v16
	v_and_b32_e32 v167, 0xffff0000, v16
	v_lshlrev_b32_e32 v16, 16, v17
	v_and_b32_e32 v17, 0xffff0000, v17
	v_lshlrev_b32_e32 v170, 16, v152
	v_and_b32_e32 v171, 0xffff0000, v152
	v_lshlrev_b32_e32 v152, 16, v153
	v_and_b32_e32 v153, 0xffff0000, v153
	v_mul_f32_e32 v6, v117, v117
	v_mul_f32_e32 v7, v115, v115
	v_pk_fma_f32 v[126:127], v[10:11], v[16:17], v[152:153]
	v_pk_fma_f32 v[128:129], v[12:13], v[166:167], v[170:171]
	v_fmac_f32_e32 v6, v116, v116
	v_fmac_f32_e32 v7, v114, v114
	v_add_f32_e32 v6, v6, v7
	v_mul_f32_e32 v7, v129, v129
	v_mul_f32_e32 v8, v127, v127
	v_fmac_f32_e32 v7, v128, v128
	v_fmac_f32_e32 v8, v126, v126
	v_add_f32_e32 v7, v7, v8
	v_add_f32_e32 v6, v6, v7
	v_add_f32_e32 v6, v156, v6
	ds_bpermute_b32 v7, v1, v6
	s_waitcnt lgkmcnt(0)
	v_add_f32_e32 v6, v6, v7
	ds_bpermute_b32 v7, v5, v6
	s_and_saveexec_b64 s[20:21], vcc
	s_cbranch_execz .LBB0_1539
	s_waitcnt lgkmcnt(0)
	v_add_f32_e32 v6, v6, v7
	ds_write_b32 v4, v6 offset:512
.LBB0_1539:
	s_or_b64 exec, exec, s[20:21]
	s_waitcnt lgkmcnt(0)
	s_waitcnt vmcnt(8)
	v_mov_b64_e32 v[6:7], v[232:233]
	v_mov_b64_e32 v[8:9], v[234:235]
	v_mov_b64_e32 v[10:11], v[236:237]
	v_mov_b64_e32 v[12:13], v[238:239]
	v_mov_b64_e32 v[14:15], v[240:241]
	v_mov_b64_e32 v[16:17], v[242:243]
	v_mov_b64_e32 v[150:151], v[244:245]
	v_mov_b64_e32 v[152:153], v[246:247]
	v_lshl_add_u64 v[254:255], v[254:255], 0, v[250:251]
	v_lshl_add_u64 v[196:197], v[196:197], 0, v[250:251]
	global_load_dwordx4 v[232:235], v[254:255], off
	global_load_dwordx4 v[236:239], v[196:197], off
	global_load_dwordx4 v[240:243], v[254:255], off offset:256
	global_load_dwordx4 v[244:247], v[196:197], off offset:256
	v_pk_mul_f32 v[112:113], v[112:113], s[6:7] op_sel_hi:[1,0]
	v_pk_mul_f32 v[110:111], v[110:111], s[6:7] op_sel_hi:[1,0]
	v_pk_mul_f32 v[108:109], v[108:109], s[6:7] op_sel_hi:[1,0]
	v_pk_mul_f32 v[106:107], v[106:107], s[6:7] op_sel_hi:[1,0]
	v_pk_mul_f32 v[104:105], v[104:105], s[6:7] op_sel_hi:[1,0]
	v_pk_mul_f32 v[110:111], v[110:111], s[2:3] op_sel_hi:[1,0]
	v_pk_mul_f32 v[112:113], v[112:113], s[2:3] op_sel_hi:[1,0]
	v_pk_mul_f32 v[106:107], v[106:107], s[2:3] op_sel_hi:[1,0]
	v_pk_mul_f32 v[108:109], v[108:109], s[2:3] op_sel_hi:[1,0]
	v_pk_mul_f32 v[154:155], v[104:105], s[2:3] op_sel_hi:[1,0]
	v_exp_f32_e32 v104, v110
	v_exp_f32_e32 v105, v111
	v_exp_f32_e32 v110, v112
	v_exp_f32_e32 v111, v113
	v_exp_f32_e32 v106, v106
	v_exp_f32_e32 v107, v107
	v_exp_f32_e32 v108, v108
	v_exp_f32_e32 v109, v109
	v_pk_mul_f32 v[102:103], v[102:103], s[6:7] op_sel_hi:[1,0]
	v_pk_add_f32 v[106:107], v[106:107], 1.0 op_sel_hi:[1,0]
	v_pk_mul_f32 v[102:103], v[102:103], s[2:3] op_sel_hi:[1,0]
	v_pk_add_f32 v[108:109], v[108:109], 1.0 op_sel_hi:[1,0]
	v_exp_f32_e32 v112, v102
	v_exp_f32_e32 v113, v103
	v_pk_add_f32 v[102:103], v[104:105], 1.0 op_sel_hi:[1,0]
	v_pk_add_f32 v[104:105], v[110:111], 1.0 op_sel_hi:[1,0]
	v_rcp_f32_e32 v102, v102
	v_rcp_f32_e32 v103, v103
	v_rcp_f32_e32 v104, v104
	v_rcp_f32_e32 v105, v105
	v_rcp_f32_e32 v110, v106
	v_rcp_f32_e32 v111, v107
	v_rcp_f32_e32 v156, v108
	v_rcp_f32_e32 v157, v109
	v_lshlrev_b32_e32 v160, 16, v10
	v_lshlrev_b32_e32 v108, 16, v6
	v_and_b32_e32 v109, 0xffff0000, v6
	v_lshlrev_b32_e32 v6, 16, v7
	v_and_b32_e32 v7, 0xffff0000, v7
	v_lshlrev_b32_e32 v158, 16, v8
	v_and_b32_e32 v159, 0xffff0000, v8
	v_lshlrev_b32_e32 v8, 16, v9
	v_and_b32_e32 v9, 0xffff0000, v9
	v_and_b32_e32 v161, 0xffff0000, v10
	v_lshlrev_b32_e32 v10, 16, v11
	v_and_b32_e32 v11, 0xffff0000, v11
	v_lshlrev_b32_e32 v162, 16, v12
	v_and_b32_e32 v163, 0xffff0000, v12
	v_lshlrev_b32_e32 v12, 16, v13
	v_and_b32_e32 v13, 0xffff0000, v13
	v_pk_fma_f32 v[106:107], v[104:105], v[6:7], v[10:11]
	v_pk_fma_f32 v[108:109], v[102:103], v[108:109], v[160:161]
	v_pk_fma_f32 v[102:103], v[156:157], v[8:9], v[12:13]
	v_pk_fma_f32 v[104:105], v[110:111], v[158:159], v[162:163]
	v_mul_f32_e32 v6, v109, v109
	v_mul_f32_e32 v7, v107, v107
	v_mul_f32_e32 v8, v105, v105
	v_mul_f32_e32 v9, v103, v103
	v_fmac_f32_e32 v6, v108, v108
	v_fmac_f32_e32 v7, v106, v106
	v_fmac_f32_e32 v8, v104, v104
	v_fmac_f32_e32 v9, v102, v102
	v_add_f32_e32 v6, v6, v7
	v_add_f32_e32 v7, v8, v9
	v_add_f32_e32 v156, v6, v7
	v_exp_f32_e32 v6, v154
	v_exp_f32_e32 v7, v155
	v_pk_mul_f32 v[10:11], v[100:101], s[6:7] op_sel_hi:[1,0]
	v_pk_mul_f32 v[12:13], v[98:99], s[6:7] op_sel_hi:[1,0]
	v_pk_mul_f32 v[10:11], v[10:11], s[2:3] op_sel_hi:[1,0]
	v_pk_mul_f32 v[12:13], v[12:13], s[2:3] op_sel_hi:[1,0]
	v_exp_f32_e32 v10, v10
	v_exp_f32_e32 v12, v12
	v_exp_f32_e32 v13, v13
	v_exp_f32_e32 v11, v11
	v_pk_add_f32 v[8:9], v[112:113], 1.0 op_sel_hi:[1,0]
	v_pk_add_f32 v[6:7], v[6:7], 1.0 op_sel_hi:[1,0]
	v_rcp_f32_e32 v8, v8
	v_rcp_f32_e32 v9, v9
	v_rcp_f32_e32 v6, v6
	v_rcp_f32_e32 v7, v7
	v_pk_add_f32 v[12:13], v[12:13], 1.0 op_sel_hi:[1,0]
	v_pk_add_f32 v[10:11], v[10:11], 1.0 op_sel_hi:[1,0]
	v_rcp_f32_e32 v12, v12
	v_rcp_f32_e32 v10, v10
	v_rcp_f32_e32 v11, v11
	v_rcp_f32_e32 v13, v13
	v_lshlrev_b32_e32 v164, 16, v14
	v_and_b32_e32 v165, 0xffff0000, v14
	v_lshlrev_b32_e32 v14, 16, v15
	v_and_b32_e32 v15, 0xffff0000, v15
	v_lshlrev_b32_e32 v168, 16, v150
	v_and_b32_e32 v169, 0xffff0000, v150
	v_lshlrev_b32_e32 v150, 16, v151
	v_and_b32_e32 v151, 0xffff0000, v151
	v_pk_fma_f32 v[100:101], v[6:7], v[14:15], v[150:151]
	v_pk_fma_f32 v[110:111], v[8:9], v[164:165], v[168:169]
	v_lshlrev_b32_e32 v166, 16, v16
	v_and_b32_e32 v167, 0xffff0000, v16
	v_lshlrev_b32_e32 v16, 16, v17
	v_and_b32_e32 v17, 0xffff0000, v17
	v_lshlrev_b32_e32 v170, 16, v152
	v_and_b32_e32 v171, 0xffff0000, v152
	v_lshlrev_b32_e32 v152, 16, v153
	v_and_b32_e32 v153, 0xffff0000, v153
	v_mul_f32_e32 v6, v111, v111
	v_mul_f32_e32 v7, v101, v101
	v_pk_fma_f32 v[98:99], v[10:11], v[16:17], v[152:153]
	v_pk_fma_f32 v[112:113], v[12:13], v[166:167], v[170:171]
	v_fmac_f32_e32 v6, v110, v110
	v_fmac_f32_e32 v7, v100, v100
	v_add_f32_e32 v6, v6, v7
	v_mul_f32_e32 v7, v113, v113
	v_mul_f32_e32 v8, v99, v99
	v_fmac_f32_e32 v7, v112, v112
	v_fmac_f32_e32 v8, v98, v98
	v_add_f32_e32 v7, v7, v8
	v_add_f32_e32 v6, v6, v7
	v_add_f32_e32 v6, v156, v6
	ds_bpermute_b32 v7, v1, v6
	s_waitcnt lgkmcnt(0)
	v_add_f32_e32 v6, v6, v7
	ds_bpermute_b32 v7, v5, v6
	s_and_saveexec_b64 s[2:3], vcc
	s_cbranch_execz .LBB0_1541
	s_waitcnt lgkmcnt(0)
	v_add_f32_e32 v6, v6, v7
	ds_write_b32 v4, v6 offset:768
.LBB0_1541:
	s_or_b64 exec, exec, s[2:3]
	s_waitcnt lgkmcnt(0)
	s_waitcnt vmcnt(8)
	v_mov_b64_e32 v[6:7], v[200:201]
	v_mov_b64_e32 v[8:9], v[202:203]
	v_mov_b64_e32 v[10:11], v[204:205]
	v_mov_b64_e32 v[12:13], v[206:207]
	v_mov_b64_e32 v[14:15], v[208:209]
	v_mov_b64_e32 v[16:17], v[210:211]
	v_mov_b64_e32 v[150:151], v[212:213]
	v_mov_b64_e32 v[152:153], v[214:215]
	v_lshl_add_u64 v[254:255], v[254:255], 0, v[250:251]
	v_lshl_add_u64 v[196:197], v[196:197], 0, v[250:251]
	global_load_dwordx4 v[200:203], v[254:255], off
	global_load_dwordx4 v[204:207], v[196:197], off
	global_load_dwordx4 v[208:211], v[254:255], off offset:256
	global_load_dwordx4 v[212:215], v[196:197], off offset:256
	s_mov_b32 s2, 0xbfb8aa3b
	v_pk_mul_f32 v[96:97], v[96:97], s[6:7] op_sel_hi:[1,0]
	v_pk_mul_f32 v[94:95], v[94:95], s[6:7] op_sel_hi:[1,0]
	v_pk_mul_f32 v[92:93], v[92:93], s[6:7] op_sel_hi:[1,0]
	v_pk_mul_f32 v[90:91], v[90:91], s[6:7] op_sel_hi:[1,0]
	v_pk_mul_f32 v[154:155], v[88:89], s[6:7] op_sel_hi:[1,0]
	v_pk_mul_f32 v[86:87], v[86:87], s[6:7] op_sel_hi:[1,0]
	v_pk_mul_f32 v[88:89], v[94:95], s[2:3] op_sel_hi:[1,0]
	v_pk_mul_f32 v[94:95], v[96:97], s[2:3] op_sel_hi:[1,0]
	v_pk_mul_f32 v[90:91], v[90:91], s[2:3] op_sel_hi:[1,0]
	v_pk_mul_f32 v[92:93], v[92:93], s[2:3] op_sel_hi:[1,0]
	v_pk_mul_f32 v[96:97], v[86:87], s[2:3] op_sel_hi:[1,0]
	v_exp_f32_e32 v86, v88
	v_exp_f32_e32 v87, v89
	v_exp_f32_e32 v88, v94
	v_exp_f32_e32 v89, v95
	v_exp_f32_e32 v90, v90
	v_exp_f32_e32 v91, v91
	v_exp_f32_e32 v92, v92
	v_exp_f32_e32 v93, v93
	v_pk_add_f32 v[86:87], v[86:87], 1.0 op_sel_hi:[1,0]
	v_pk_add_f32 v[88:89], v[88:89], 1.0 op_sel_hi:[1,0]
	v_pk_add_f32 v[90:91], v[90:91], 1.0 op_sel_hi:[1,0]
	v_pk_add_f32 v[92:93], v[92:93], 1.0 op_sel_hi:[1,0]
	v_rcp_f32_e32 v86, v86
	v_rcp_f32_e32 v87, v87
	v_rcp_f32_e32 v88, v88
	v_rcp_f32_e32 v89, v89
	v_rcp_f32_e32 v94, v90
	v_rcp_f32_e32 v95, v91
	v_rcp_f32_e32 v156, v92
	v_rcp_f32_e32 v157, v93
	v_lshlrev_b32_e32 v160, 16, v10
	v_lshlrev_b32_e32 v92, 16, v6
	v_and_b32_e32 v93, 0xffff0000, v6
	v_lshlrev_b32_e32 v6, 16, v7
	v_and_b32_e32 v7, 0xffff0000, v7
	v_lshlrev_b32_e32 v158, 16, v8
	v_and_b32_e32 v159, 0xffff0000, v8
	v_lshlrev_b32_e32 v8, 16, v9
	v_and_b32_e32 v9, 0xffff0000, v9
	v_and_b32_e32 v161, 0xffff0000, v10
	v_lshlrev_b32_e32 v10, 16, v11
	v_and_b32_e32 v11, 0xffff0000, v11
	v_lshlrev_b32_e32 v162, 16, v12
	v_and_b32_e32 v163, 0xffff0000, v12
	v_lshlrev_b32_e32 v12, 16, v13
	v_and_b32_e32 v13, 0xffff0000, v13
	v_pk_fma_f32 v[90:91], v[88:89], v[6:7], v[10:11]
	v_pk_fma_f32 v[92:93], v[86:87], v[92:93], v[160:161]
	v_pk_fma_f32 v[86:87], v[156:157], v[8:9], v[12:13]
	v_pk_fma_f32 v[88:89], v[94:95], v[158:159], v[162:163]
	v_mul_f32_e32 v6, v93, v93
	v_mul_f32_e32 v7, v91, v91
	v_mul_f32_e32 v8, v89, v89
	v_mul_f32_e32 v9, v87, v87
	v_fmac_f32_e32 v6, v92, v92
	v_fmac_f32_e32 v7, v90, v90
	v_fmac_f32_e32 v8, v88, v88
	v_fmac_f32_e32 v9, v86, v86
	v_add_f32_e32 v6, v6, v7
	v_add_f32_e32 v7, v8, v9
	v_pk_mul_f32 v[8:9], v[154:155], s[2:3] op_sel_hi:[1,0]
	v_add_f32_e32 v19, v6, v7
	v_exp_f32_e32 v6, v96
	v_exp_f32_e32 v7, v97
	v_exp_f32_e32 v8, v8
	v_exp_f32_e32 v9, v9
	v_pk_mul_f32 v[10:11], v[84:85], s[6:7] op_sel_hi:[1,0]
	v_pk_mul_f32 v[12:13], v[82:83], s[6:7] op_sel_hi:[1,0]
	v_pk_mul_f32 v[10:11], v[10:11], s[2:3] op_sel_hi:[1,0]
	v_pk_mul_f32 v[12:13], v[12:13], s[2:3] op_sel_hi:[1,0]
	v_exp_f32_e32 v10, v10
	v_exp_f32_e32 v12, v12
	v_exp_f32_e32 v13, v13
	v_exp_f32_e32 v11, v11
	v_pk_add_f32 v[6:7], v[6:7], 1.0 op_sel_hi:[1,0]
	v_pk_add_f32 v[8:9], v[8:9], 1.0 op_sel_hi:[1,0]
	v_rcp_f32_e32 v6, v6
	v_rcp_f32_e32 v7, v7
	v_rcp_f32_e32 v8, v8
	v_rcp_f32_e32 v9, v9
	v_pk_add_f32 v[12:13], v[12:13], 1.0 op_sel_hi:[1,0]
	v_pk_add_f32 v[10:11], v[10:11], 1.0 op_sel_hi:[1,0]
	v_rcp_f32_e32 v12, v12
	v_rcp_f32_e32 v10, v10
	v_rcp_f32_e32 v11, v11
	v_rcp_f32_e32 v13, v13
	v_lshlrev_b32_e32 v164, 16, v14
	v_and_b32_e32 v165, 0xffff0000, v14
	v_lshlrev_b32_e32 v14, 16, v15
	v_and_b32_e32 v15, 0xffff0000, v15
	v_lshlrev_b32_e32 v168, 16, v150
	v_and_b32_e32 v169, 0xffff0000, v150
	v_lshlrev_b32_e32 v150, 16, v151
	v_and_b32_e32 v151, 0xffff0000, v151
	v_pk_fma_f32 v[84:85], v[8:9], v[14:15], v[150:151]
	v_pk_fma_f32 v[94:95], v[6:7], v[164:165], v[168:169]
	v_lshlrev_b32_e32 v166, 16, v16
	v_and_b32_e32 v167, 0xffff0000, v16
	v_lshlrev_b32_e32 v16, 16, v17
	v_and_b32_e32 v17, 0xffff0000, v17
	v_lshlrev_b32_e32 v170, 16, v152
	v_and_b32_e32 v171, 0xffff0000, v152
	v_lshlrev_b32_e32 v152, 16, v153
	v_and_b32_e32 v153, 0xffff0000, v153
	v_mul_f32_e32 v6, v95, v95
	v_mul_f32_e32 v7, v85, v85
	v_pk_fma_f32 v[82:83], v[10:11], v[16:17], v[152:153]
	v_pk_fma_f32 v[96:97], v[12:13], v[166:167], v[170:171]
	v_fmac_f32_e32 v6, v94, v94
	v_fmac_f32_e32 v7, v84, v84
	v_add_f32_e32 v6, v6, v7
	v_mul_f32_e32 v7, v97, v97
	v_mul_f32_e32 v8, v83, v83
	v_fmac_f32_e32 v7, v96, v96
	v_fmac_f32_e32 v8, v82, v82
	v_add_f32_e32 v7, v7, v8
	v_add_f32_e32 v6, v6, v7
	v_add_f32_e32 v6, v19, v6
	ds_bpermute_b32 v7, v1, v6
	v_add_u32_e32 v19, 0x80, v189
	s_waitcnt lgkmcnt(0)
	v_add_f32_e32 v6, v6, v7
	ds_bpermute_b32 v7, v5, v6
	s_and_saveexec_b64 s[20:21], vcc
	s_cbranch_execz .LBB0_1543
	v_lshl_add_u32 v8, v19, 4, s5
	s_waitcnt lgkmcnt(0)
	v_add_f32_e32 v6, v6, v7
	ds_write_b32 v8, v6
.LBB0_1543:
	s_or_b64 exec, exec, s[20:21]
	v_add_u32_e32 v150, 0x90, v18
	v_ashrrev_i32_e32 v151, 31, v150
	s_waitcnt lgkmcnt(0)
	s_waitcnt vmcnt(8)
	v_mov_b64_e32 v[6:7], v[216:217]
	v_mov_b64_e32 v[8:9], v[218:219]
	v_mov_b64_e32 v[10:11], v[220:221]
	v_mov_b64_e32 v[12:13], v[222:223]
	v_mov_b64_e32 v[14:15], v[224:225]
	v_mov_b64_e32 v[16:17], v[226:227]
	v_mov_b64_e32 v[152:153], v[228:229]
	v_mov_b64_e32 v[154:155], v[230:231]
	v_pk_mul_f32 v[80:81], v[80:81], s[6:7] op_sel_hi:[1,0]
	v_pk_mul_f32 v[78:79], v[78:79], s[6:7] op_sel_hi:[1,0]
	v_pk_mul_f32 v[76:77], v[76:77], s[6:7] op_sel_hi:[1,0]
	v_pk_mul_f32 v[74:75], v[74:75], s[6:7] op_sel_hi:[1,0]
	v_pk_mul_f32 v[72:73], v[72:73], s[6:7] op_sel_hi:[1,0]
	v_pk_mul_f32 v[78:79], v[78:79], s[2:3] op_sel_hi:[1,0]
	v_pk_mul_f32 v[80:81], v[80:81], s[2:3] op_sel_hi:[1,0]
	v_pk_mul_f32 v[74:75], v[74:75], s[2:3] op_sel_hi:[1,0]
	v_pk_mul_f32 v[76:77], v[76:77], s[2:3] op_sel_hi:[1,0]
	v_pk_mul_f32 v[156:157], v[72:73], s[2:3] op_sel_hi:[1,0]
	v_exp_f32_e32 v72, v78
	v_exp_f32_e32 v73, v79
	v_exp_f32_e32 v78, v80
	v_exp_f32_e32 v79, v81
	v_exp_f32_e32 v74, v74
	v_exp_f32_e32 v75, v75
	v_exp_f32_e32 v76, v76
	v_exp_f32_e32 v77, v77
	v_pk_mul_f32 v[70:71], v[70:71], s[6:7] op_sel_hi:[1,0]
	v_pk_add_f32 v[74:75], v[74:75], 1.0 op_sel_hi:[1,0]
	v_pk_mul_f32 v[70:71], v[70:71], s[2:3] op_sel_hi:[1,0]
	v_pk_add_f32 v[76:77], v[76:77], 1.0 op_sel_hi:[1,0]
	v_exp_f32_e32 v80, v70
	v_exp_f32_e32 v81, v71
	v_pk_add_f32 v[70:71], v[72:73], 1.0 op_sel_hi:[1,0]
	v_pk_add_f32 v[72:73], v[78:79], 1.0 op_sel_hi:[1,0]
	v_rcp_f32_e32 v70, v70
	v_rcp_f32_e32 v71, v71
	v_rcp_f32_e32 v72, v72
	v_rcp_f32_e32 v73, v73
	v_rcp_f32_e32 v78, v74
	v_rcp_f32_e32 v79, v75
	v_rcp_f32_e32 v158, v76
	v_rcp_f32_e32 v159, v77
	v_lshlrev_b32_e32 v162, 16, v10
	v_lshlrev_b32_e32 v76, 16, v6
	v_and_b32_e32 v77, 0xffff0000, v6
	v_lshlrev_b32_e32 v6, 16, v7
	v_and_b32_e32 v7, 0xffff0000, v7
	v_lshlrev_b32_e32 v160, 16, v8
	v_and_b32_e32 v161, 0xffff0000, v8
	v_lshlrev_b32_e32 v8, 16, v9
	v_and_b32_e32 v9, 0xffff0000, v9
	v_and_b32_e32 v163, 0xffff0000, v10
	v_lshlrev_b32_e32 v10, 16, v11
	v_and_b32_e32 v11, 0xffff0000, v11
	v_lshlrev_b32_e32 v164, 16, v12
	v_and_b32_e32 v165, 0xffff0000, v12
	v_lshlrev_b32_e32 v12, 16, v13
	v_and_b32_e32 v13, 0xffff0000, v13
	v_pk_fma_f32 v[74:75], v[72:73], v[6:7], v[10:11]
	v_pk_fma_f32 v[76:77], v[70:71], v[76:77], v[162:163]
	v_pk_fma_f32 v[70:71], v[158:159], v[8:9], v[12:13]
	v_pk_fma_f32 v[72:73], v[78:79], v[160:161], v[164:165]
	v_mul_f32_e32 v6, v77, v77
	v_mul_f32_e32 v7, v75, v75
	v_mul_f32_e32 v8, v73, v73
	v_mul_f32_e32 v9, v71, v71
	v_fmac_f32_e32 v6, v76, v76
	v_fmac_f32_e32 v7, v74, v74
	v_fmac_f32_e32 v8, v72, v72
	v_fmac_f32_e32 v9, v70, v70
	v_add_f32_e32 v6, v6, v7
	v_add_f32_e32 v7, v8, v9
	v_add_f32_e32 v158, v6, v7
	v_exp_f32_e32 v6, v156
	v_exp_f32_e32 v7, v157
	v_pk_mul_f32 v[10:11], v[68:69], s[6:7] op_sel_hi:[1,0]
	v_pk_mul_f32 v[12:13], v[66:67], s[6:7] op_sel_hi:[1,0]
	v_pk_mul_f32 v[10:11], v[10:11], s[2:3] op_sel_hi:[1,0]
	v_pk_mul_f32 v[12:13], v[12:13], s[2:3] op_sel_hi:[1,0]
	v_exp_f32_e32 v10, v10
	v_exp_f32_e32 v12, v12
	v_exp_f32_e32 v13, v13
	v_exp_f32_e32 v11, v11
	v_pk_add_f32 v[8:9], v[80:81], 1.0 op_sel_hi:[1,0]
	v_pk_add_f32 v[6:7], v[6:7], 1.0 op_sel_hi:[1,0]
	v_rcp_f32_e32 v8, v8
	v_rcp_f32_e32 v9, v9
	v_rcp_f32_e32 v6, v6
	v_rcp_f32_e32 v7, v7
	v_pk_add_f32 v[12:13], v[12:13], 1.0 op_sel_hi:[1,0]
	v_pk_add_f32 v[10:11], v[10:11], 1.0 op_sel_hi:[1,0]
	v_rcp_f32_e32 v12, v12
	v_rcp_f32_e32 v10, v10
	v_rcp_f32_e32 v11, v11
	v_rcp_f32_e32 v13, v13
	v_lshlrev_b32_e32 v166, 16, v14
	v_and_b32_e32 v167, 0xffff0000, v14
	v_lshlrev_b32_e32 v14, 16, v15
	v_and_b32_e32 v15, 0xffff0000, v15
	v_lshlrev_b32_e32 v170, 16, v152
	v_and_b32_e32 v171, 0xffff0000, v152
	v_lshlrev_b32_e32 v152, 16, v153
	v_and_b32_e32 v153, 0xffff0000, v153
	v_pk_fma_f32 v[68:69], v[6:7], v[14:15], v[152:153]
	v_pk_fma_f32 v[78:79], v[8:9], v[166:167], v[170:171]
	v_lshlrev_b32_e32 v168, 16, v16
	v_and_b32_e32 v169, 0xffff0000, v16
	v_lshlrev_b32_e32 v16, 16, v17
	v_and_b32_e32 v17, 0xffff0000, v17
	v_lshlrev_b32_e32 v172, 16, v154
	v_and_b32_e32 v173, 0xffff0000, v154
	v_lshlrev_b32_e32 v154, 16, v155
	v_and_b32_e32 v155, 0xffff0000, v155
	v_mul_f32_e32 v6, v79, v79
	v_mul_f32_e32 v7, v69, v69
	v_pk_fma_f32 v[66:67], v[10:11], v[16:17], v[154:155]
	v_pk_fma_f32 v[80:81], v[12:13], v[168:169], v[172:173]
	v_fmac_f32_e32 v6, v78, v78
	v_fmac_f32_e32 v7, v68, v68
	v_add_f32_e32 v6, v6, v7
	v_mul_f32_e32 v7, v81, v81
	v_mul_f32_e32 v8, v67, v67
	v_fmac_f32_e32 v7, v80, v80
	v_fmac_f32_e32 v8, v66, v66
	v_add_f32_e32 v7, v7, v8
	v_add_f32_e32 v6, v6, v7
	v_add_f32_e32 v6, v158, v6
	ds_bpermute_b32 v7, v1, v6
	s_waitcnt lgkmcnt(0)
	v_add_f32_e32 v6, v6, v7
	ds_bpermute_b32 v7, v5, v6
	s_and_saveexec_b64 s[2:3], vcc
	s_cbranch_execz .LBB0_1545
	s_waitcnt lgkmcnt(0)
	v_add_f32_e32 v6, v6, v7
	ds_write_b32 v4, v6 offset:2304
.LBB0_1545:
	s_or_b64 exec, exec, s[2:3]
	v_add_u32_e32 v152, 0xa0, v18
	v_ashrrev_i32_e32 v153, 31, v152
	s_waitcnt lgkmcnt(0)
	s_waitcnt vmcnt(4)
	v_mov_b64_e32 v[6:7], v[232:233]
	v_mov_b64_e32 v[8:9], v[234:235]
	v_mov_b64_e32 v[10:11], v[236:237]
	v_mov_b64_e32 v[12:13], v[238:239]
	v_mov_b64_e32 v[14:15], v[240:241]
	v_mov_b64_e32 v[16:17], v[242:243]
	v_mov_b64_e32 v[154:155], v[244:245]
	v_mov_b64_e32 v[156:157], v[246:247]
	s_mov_b32 s2, 0xbfb8aa3b
	v_pk_mul_f32 v[64:65], v[64:65], s[6:7] op_sel_hi:[1,0]
	v_pk_mul_f32 v[62:63], v[62:63], s[6:7] op_sel_hi:[1,0]
	v_pk_mul_f32 v[60:61], v[60:61], s[6:7] op_sel_hi:[1,0]
	v_pk_mul_f32 v[58:59], v[58:59], s[6:7] op_sel_hi:[1,0]
	v_pk_mul_f32 v[158:159], v[56:57], s[6:7] op_sel_hi:[1,0]
	v_pk_mul_f32 v[54:55], v[54:55], s[6:7] op_sel_hi:[1,0]
	v_pk_mul_f32 v[56:57], v[62:63], s[2:3] op_sel_hi:[1,0]
	v_pk_mul_f32 v[62:63], v[64:65], s[2:3] op_sel_hi:[1,0]
	v_pk_mul_f32 v[58:59], v[58:59], s[2:3] op_sel_hi:[1,0]
	v_pk_mul_f32 v[60:61], v[60:61], s[2:3] op_sel_hi:[1,0]
	v_pk_mul_f32 v[64:65], v[54:55], s[2:3] op_sel_hi:[1,0]
	v_exp_f32_e32 v54, v56
	v_exp_f32_e32 v55, v57
	v_exp_f32_e32 v56, v62
	v_exp_f32_e32 v57, v63
	v_exp_f32_e32 v58, v58
	v_exp_f32_e32 v59, v59
	v_exp_f32_e32 v60, v60
	v_exp_f32_e32 v61, v61
	v_pk_add_f32 v[54:55], v[54:55], 1.0 op_sel_hi:[1,0]
	v_pk_add_f32 v[56:57], v[56:57], 1.0 op_sel_hi:[1,0]
	v_pk_add_f32 v[58:59], v[58:59], 1.0 op_sel_hi:[1,0]
	v_pk_add_f32 v[60:61], v[60:61], 1.0 op_sel_hi:[1,0]
	v_rcp_f32_e32 v54, v54
	v_rcp_f32_e32 v55, v55
	v_rcp_f32_e32 v56, v56
	v_rcp_f32_e32 v57, v57
	v_rcp_f32_e32 v160, v58
	v_rcp_f32_e32 v161, v59
	v_rcp_f32_e32 v162, v60
	v_rcp_f32_e32 v163, v61
	v_exp_f32_e32 v62, v64
	v_exp_f32_e32 v63, v65
	v_lshlrev_b32_e32 v166, 16, v10
	v_lshlrev_b32_e32 v60, 16, v6
	v_and_b32_e32 v61, 0xffff0000, v6
	v_lshlrev_b32_e32 v6, 16, v7
	v_and_b32_e32 v7, 0xffff0000, v7
	v_lshlrev_b32_e32 v164, 16, v8
	v_and_b32_e32 v165, 0xffff0000, v8
	v_lshlrev_b32_e32 v8, 16, v9
	v_and_b32_e32 v9, 0xffff0000, v9
	v_and_b32_e32 v167, 0xffff0000, v10
	v_lshlrev_b32_e32 v10, 16, v11
	v_and_b32_e32 v11, 0xffff0000, v11
	v_lshlrev_b32_e32 v168, 16, v12
	v_and_b32_e32 v169, 0xffff0000, v12
	v_lshlrev_b32_e32 v12, 16, v13
	v_and_b32_e32 v13, 0xffff0000, v13
	v_pk_fma_f32 v[58:59], v[56:57], v[6:7], v[10:11]
	v_pk_fma_f32 v[60:61], v[54:55], v[60:61], v[166:167]
	v_pk_fma_f32 v[54:55], v[162:163], v[8:9], v[12:13]
	v_pk_fma_f32 v[56:57], v[160:161], v[164:165], v[168:169]
	v_mul_f32_e32 v6, v61, v61
	v_mul_f32_e32 v7, v59, v59
	v_mul_f32_e32 v8, v57, v57
	v_mul_f32_e32 v9, v55, v55
	v_fmac_f32_e32 v6, v60, v60
	v_fmac_f32_e32 v7, v58, v58
	v_fmac_f32_e32 v8, v56, v56
	v_fmac_f32_e32 v9, v54, v54
	v_add_f32_e32 v6, v6, v7
	v_add_f32_e32 v7, v8, v9
	v_add_f32_e32 v160, v6, v7
	v_pk_mul_f32 v[6:7], v[158:159], s[2:3] op_sel_hi:[1,0]
	v_pk_mul_f32 v[10:11], v[52:53], s[6:7] op_sel_hi:[1,0]
	v_exp_f32_e32 v6, v6
	v_exp_f32_e32 v7, v7
	v_pk_mul_f32 v[12:13], v[50:51], s[6:7] op_sel_hi:[1,0]
	v_pk_mul_f32 v[10:11], v[10:11], s[2:3] op_sel_hi:[1,0]
	v_pk_mul_f32 v[12:13], v[12:13], s[2:3] op_sel_hi:[1,0]
	v_exp_f32_e32 v10, v10
	v_exp_f32_e32 v12, v12
	v_exp_f32_e32 v13, v13
	v_exp_f32_e32 v11, v11
	v_pk_add_f32 v[8:9], v[62:63], 1.0 op_sel_hi:[1,0]
	v_pk_add_f32 v[6:7], v[6:7], 1.0 op_sel_hi:[1,0]
	v_rcp_f32_e32 v8, v8
	v_rcp_f32_e32 v9, v9
	v_rcp_f32_e32 v6, v6
	v_rcp_f32_e32 v7, v7
	v_pk_add_f32 v[12:13], v[12:13], 1.0 op_sel_hi:[1,0]
	v_pk_add_f32 v[10:11], v[10:11], 1.0 op_sel_hi:[1,0]
	v_rcp_f32_e32 v12, v12
	v_rcp_f32_e32 v10, v10
	v_rcp_f32_e32 v11, v11
	v_rcp_f32_e32 v13, v13
	v_lshlrev_b32_e32 v170, 16, v14
	v_and_b32_e32 v171, 0xffff0000, v14
	v_lshlrev_b32_e32 v14, 16, v15
	v_and_b32_e32 v15, 0xffff0000, v15
	v_lshlrev_b32_e32 v174, 16, v154
	v_and_b32_e32 v175, 0xffff0000, v154
	v_lshlrev_b32_e32 v154, 16, v155
	v_and_b32_e32 v155, 0xffff0000, v155
	v_pk_fma_f32 v[52:53], v[6:7], v[14:15], v[154:155]
	v_pk_fma_f32 v[62:63], v[8:9], v[170:171], v[174:175]
	v_lshlrev_b32_e32 v172, 16, v16
	v_and_b32_e32 v173, 0xffff0000, v16
	v_lshlrev_b32_e32 v16, 16, v17
	v_and_b32_e32 v17, 0xffff0000, v17
	v_lshlrev_b32_e32 v176, 16, v156
	v_and_b32_e32 v177, 0xffff0000, v156
	v_lshlrev_b32_e32 v156, 16, v157
	v_and_b32_e32 v157, 0xffff0000, v157
	v_mul_f32_e32 v6, v63, v63
	v_mul_f32_e32 v7, v53, v53
	v_pk_fma_f32 v[50:51], v[10:11], v[16:17], v[156:157]
	v_pk_fma_f32 v[64:65], v[12:13], v[172:173], v[176:177]
	v_fmac_f32_e32 v6, v62, v62
	v_fmac_f32_e32 v7, v52, v52
	v_add_f32_e32 v6, v6, v7
	v_mul_f32_e32 v7, v65, v65
	v_mul_f32_e32 v8, v51, v51
	v_fmac_f32_e32 v7, v64, v64
	v_fmac_f32_e32 v8, v50, v50
	v_add_f32_e32 v7, v7, v8
	v_add_f32_e32 v6, v6, v7
	v_add_f32_e32 v6, v160, v6
	ds_bpermute_b32 v7, v1, v6
	s_waitcnt lgkmcnt(0)
	v_add_f32_e32 v6, v6, v7
	ds_bpermute_b32 v7, v5, v6
	s_and_saveexec_b64 s[20:21], vcc
	s_cbranch_execz .LBB0_1547
	s_waitcnt lgkmcnt(0)
	v_add_f32_e32 v6, v6, v7
	ds_write_b32 v4, v6 offset:2560
.LBB0_1547:
	s_or_b64 exec, exec, s[20:21]
	v_add_u32_e32 v154, 0xb0, v18
	v_ashrrev_i32_e32 v155, 31, v154
	s_waitcnt lgkmcnt(0)
	s_waitcnt vmcnt(0)
	v_mov_b64_e32 v[6:7], v[200:201]
	v_mov_b64_e32 v[8:9], v[202:203]
	v_mov_b64_e32 v[10:11], v[204:205]
	v_mov_b64_e32 v[12:13], v[206:207]
	v_mov_b64_e32 v[14:15], v[208:209]
	v_mov_b64_e32 v[16:17], v[210:211]
	v_mov_b64_e32 v[156:157], v[212:213]
	v_mov_b64_e32 v[158:159], v[214:215]
	v_pk_mul_f32 v[48:49], v[48:49], s[6:7] op_sel_hi:[1,0]
	v_pk_mul_f32 v[46:47], v[46:47], s[6:7] op_sel_hi:[1,0]
	v_pk_mul_f32 v[44:45], v[44:45], s[6:7] op_sel_hi:[1,0]
	v_pk_mul_f32 v[42:43], v[42:43], s[6:7] op_sel_hi:[1,0]
	v_pk_mul_f32 v[40:41], v[40:41], s[6:7] op_sel_hi:[1,0]
	v_pk_mul_f32 v[46:47], v[46:47], s[2:3] op_sel_hi:[1,0]
	v_pk_mul_f32 v[48:49], v[48:49], s[2:3] op_sel_hi:[1,0]
	v_pk_mul_f32 v[42:43], v[42:43], s[2:3] op_sel_hi:[1,0]
	v_pk_mul_f32 v[44:45], v[44:45], s[2:3] op_sel_hi:[1,0]
	v_pk_mul_f32 v[160:161], v[40:41], s[2:3] op_sel_hi:[1,0]
	v_exp_f32_e32 v40, v46
	v_exp_f32_e32 v41, v47
	v_exp_f32_e32 v46, v48
	v_exp_f32_e32 v47, v49
	v_exp_f32_e32 v42, v42
	v_exp_f32_e32 v43, v43
	v_exp_f32_e32 v44, v44
	v_exp_f32_e32 v45, v45
	v_pk_mul_f32 v[38:39], v[38:39], s[6:7] op_sel_hi:[1,0]
	v_pk_add_f32 v[42:43], v[42:43], 1.0 op_sel_hi:[1,0]
	v_pk_mul_f32 v[38:39], v[38:39], s[2:3] op_sel_hi:[1,0]
	v_pk_add_f32 v[44:45], v[44:45], 1.0 op_sel_hi:[1,0]
	v_exp_f32_e32 v48, v38
	v_exp_f32_e32 v49, v39
	v_pk_add_f32 v[38:39], v[40:41], 1.0 op_sel_hi:[1,0]
	v_pk_add_f32 v[40:41], v[46:47], 1.0 op_sel_hi:[1,0]
	v_rcp_f32_e32 v38, v38
	v_rcp_f32_e32 v39, v39
	v_rcp_f32_e32 v40, v40
	v_rcp_f32_e32 v41, v41
	v_rcp_f32_e32 v46, v42
	v_rcp_f32_e32 v47, v43
	v_rcp_f32_e32 v162, v44
	v_rcp_f32_e32 v163, v45
	v_lshlrev_b32_e32 v166, 16, v10
	v_lshlrev_b32_e32 v44, 16, v6
	v_and_b32_e32 v45, 0xffff0000, v6
	v_lshlrev_b32_e32 v6, 16, v7
	v_and_b32_e32 v7, 0xffff0000, v7
	v_lshlrev_b32_e32 v164, 16, v8
	v_and_b32_e32 v165, 0xffff0000, v8
	v_lshlrev_b32_e32 v8, 16, v9
	v_and_b32_e32 v9, 0xffff0000, v9
	v_and_b32_e32 v167, 0xffff0000, v10
	v_lshlrev_b32_e32 v10, 16, v11
	v_and_b32_e32 v11, 0xffff0000, v11
	v_lshlrev_b32_e32 v168, 16, v12
	v_and_b32_e32 v169, 0xffff0000, v12
	v_lshlrev_b32_e32 v12, 16, v13
	v_and_b32_e32 v13, 0xffff0000, v13
	v_pk_fma_f32 v[42:43], v[40:41], v[6:7], v[10:11]
	v_pk_fma_f32 v[44:45], v[38:39], v[44:45], v[166:167]
	v_pk_fma_f32 v[38:39], v[162:163], v[8:9], v[12:13]
	v_pk_fma_f32 v[40:41], v[46:47], v[164:165], v[168:169]
	v_mul_f32_e32 v6, v45, v45
	v_mul_f32_e32 v7, v43, v43
	v_mul_f32_e32 v8, v41, v41
	v_mul_f32_e32 v9, v39, v39
	v_fmac_f32_e32 v6, v44, v44
	v_fmac_f32_e32 v7, v42, v42
	v_fmac_f32_e32 v8, v40, v40
	v_fmac_f32_e32 v9, v38, v38
	v_add_f32_e32 v6, v6, v7
	v_add_f32_e32 v7, v8, v9
	v_add_f32_e32 v162, v6, v7
	v_exp_f32_e32 v6, v160
	v_exp_f32_e32 v7, v161
	v_pk_mul_f32 v[10:11], v[36:37], s[6:7] op_sel_hi:[1,0]
	v_pk_mul_f32 v[12:13], v[34:35], s[6:7] op_sel_hi:[1,0]
	v_pk_mul_f32 v[10:11], v[10:11], s[2:3] op_sel_hi:[1,0]
	v_pk_mul_f32 v[12:13], v[12:13], s[2:3] op_sel_hi:[1,0]
	v_exp_f32_e32 v10, v10
	v_exp_f32_e32 v12, v12
	v_exp_f32_e32 v13, v13
	v_exp_f32_e32 v11, v11
	v_pk_add_f32 v[8:9], v[48:49], 1.0 op_sel_hi:[1,0]
	v_pk_add_f32 v[6:7], v[6:7], 1.0 op_sel_hi:[1,0]
	v_rcp_f32_e32 v8, v8
	v_rcp_f32_e32 v9, v9
	v_rcp_f32_e32 v6, v6
	v_rcp_f32_e32 v7, v7
	v_pk_add_f32 v[12:13], v[12:13], 1.0 op_sel_hi:[1,0]
	v_pk_add_f32 v[10:11], v[10:11], 1.0 op_sel_hi:[1,0]
	v_rcp_f32_e32 v12, v12
	v_rcp_f32_e32 v10, v10
	v_rcp_f32_e32 v11, v11
	v_rcp_f32_e32 v13, v13
	v_lshlrev_b32_e32 v170, 16, v14
	v_and_b32_e32 v171, 0xffff0000, v14
	v_lshlrev_b32_e32 v14, 16, v15
	v_and_b32_e32 v15, 0xffff0000, v15
	v_lshlrev_b32_e32 v174, 16, v156
	v_and_b32_e32 v175, 0xffff0000, v156
	v_lshlrev_b32_e32 v156, 16, v157
	v_and_b32_e32 v157, 0xffff0000, v157
	v_pk_fma_f32 v[36:37], v[6:7], v[14:15], v[156:157]
	v_pk_fma_f32 v[46:47], v[8:9], v[170:171], v[174:175]
	v_lshlrev_b32_e32 v172, 16, v16
	v_and_b32_e32 v173, 0xffff0000, v16
	v_lshlrev_b32_e32 v16, 16, v17
	v_and_b32_e32 v17, 0xffff0000, v17
	v_lshlrev_b32_e32 v176, 16, v158
	v_and_b32_e32 v177, 0xffff0000, v158
	v_lshlrev_b32_e32 v158, 16, v159
	v_and_b32_e32 v159, 0xffff0000, v159
	v_mul_f32_e32 v6, v47, v47
	v_mul_f32_e32 v7, v37, v37
	v_pk_fma_f32 v[34:35], v[10:11], v[16:17], v[158:159]
	v_pk_fma_f32 v[48:49], v[12:13], v[172:173], v[176:177]
	v_fmac_f32_e32 v6, v46, v46
	v_fmac_f32_e32 v7, v36, v36
	v_add_f32_e32 v6, v6, v7
	v_mul_f32_e32 v7, v49, v49
	v_mul_f32_e32 v8, v35, v35
	v_fmac_f32_e32 v7, v48, v48
	v_fmac_f32_e32 v8, v34, v34
	v_add_f32_e32 v7, v7, v8
	v_add_f32_e32 v6, v6, v7
	v_add_f32_e32 v6, v162, v6
	ds_bpermute_b32 v1, v1, v6
	s_waitcnt lgkmcnt(0)
	v_add_f32_e32 v1, v6, v1
	ds_bpermute_b32 v5, v5, v1
	s_and_saveexec_b64 s[2:3], vcc
	s_cbranch_execz .LBB0_1549
	s_waitcnt lgkmcnt(0)
	v_add_f32_e32 v1, v1, v5
	ds_write_b32 v4, v1 offset:2816
